# P8 expert gate_up GEMM: s_setprio flipped (loader segment prio 1, MFMA segment prio 0)
# speedup vs baseline: 1.0010x; 1.0010x over previous
;     ...
;         for (int t = 0; t < nt; t += 2) {
;             const bool last = (t == nt - 2);
;             if constexpr (Sched::kGather) {
;                 if (t == 2 && has_next) {
;                     if constexpr (HM) asm volatile("s_waitcnt vmcnt(12)" : "+v"(gtok0), "+v"(gtok1), "+v"(gtok2), "+v"(gtok3) :: "memory");
;                     else asm volatile("s_waitcnt vmcnt(16)" : "+v"(gtok0), "+v"(gtok1), "+v"(gtok2), "+v"(gtok3) :: "memory");
;                     PG8_RC(); *(LAS u32x4*)(S.aux + tid * 16) = (u32x4){(unsigned)(((int)gtok0 >> 2) * S.lda + C[0]) * 2u, (unsigned)(((int)gtok1 >> 2) * S.lda + C[1]) * 2u, (unsigned)(((int)gtok2 >> 2) * S.lda + C[0]) * 2u, (unsigned)(((int)gtok3 >> 2) * S.lda + C[1]) * 2u};
;                 }
;             }
;             const char* a1 = cA + (size_t)(t + 1) * kstep;
;             const char* a2 = last ? nA : cA + (size_t)(t + 2) * kstep; const char* b2 = last ? nB : cB + (size_t)(t + 2) * kstep;
;             const char* a3 = a2 + kstep; const char* b3 = b2 + kstep;
;             PG8_LDB(B0, 0, 0); PG8_LDB(B1, 0, 1); PG8_SCHED; PG8_LDA(At, 0, 0); if constexpr (!HM) PG8_STAGEA(PG8_SA(1, 1), a1, 1);
;             if constexpr (Sched::kGather) { if (last && has_next) { const u32x4 tn = *(const LAS u32x4*)(S.aux + tid * 16); voffA[0][0] = tn.x; voffA[0][1] = tn.y; voffA[1][0] = tn.z; voffA[1][1] = tn.w; } }
;             PG8_WAIT_K0(); PG8_WAIT_L(0); PG8_BAR; PG8_MMA(0, 0, At, B0); PG8_MMA(0, 1, At, B1); PG8_BAR; PG8_SCHED;
;             if constexpr (!HM) PG8_LDA(At, 0, 1);
;             PG8_STAGEB(PG8_SB(0, 0), b2); PG8_STAGEB(PG8_SB(0, 1), b2 + hstepB); PG8_STAGEAS(PG8_SA(0, 0), a2, 0);
;             PG8_WAIT_K0(); PG8_WAIT_L(0); PG8_BAR; if constexpr (!HM) { PG8_MMA(1, 0, At, B0); PG8_MMA(1, 1, At, B1); } PG8_BAR; PG8_SCHED;
;             PG8_LDB(B0, 1, 0); PG8_LDB(B1, 1, 1); PG8_SCHED; PG8_LDA(At, 1, 0); if constexpr (!HM) PG8_STAGEAS(PG8_SA(0, 1), a2, 1);
;             PG8_WAIT_K(); PG8_WAIT_L(0); PG8_BAR; PG8_MMA(0, 0, At, B0); PG8_MMA(0, 1, At, B1); PG8_BAR; PG8_SCHED;
;             if constexpr (!HM) PG8_LDA(At, 1, 1);
;             PG8_STAGEB(PG8_SB(1, 0), b3); PG8_STAGEB(PG8_SB(1, 1), b3 + hstepB); PG8_STAGEAS(PG8_SA(1, 0), a3, 0);
;             PG8_WAIT_K(); PG8_WAIT_L(0); PG8_BAR; if constexpr (!HM) { PG8_MMA(1, 0, At, B0); PG8_MMA(1, 1, At, B1); } PG8_BAR; PG8_SCHED;
.LBB0_1131:
	s_waitcnt lgkmcnt(0)
	s_add_u32 s18, s48, 0x100
	s_addc_u32 s19, s49, 0
	s_barrier
	s_setprio 0
	v_mov_b64_e32 v[100:101], s[14:15]
	v_mov_b64_e32 v[172:173], s[14:15]
	v_mov_b64_e32 v[168:169], s[14:15]
	v_mov_b64_e32 v[156:157], s[14:15]
	v_mov_b64_e32 v[152:153], s[14:15]
	v_mov_b64_e32 v[144:145], s[14:15]
	v_mov_b64_e32 v[136:137], s[14:15]
	v_mov_b64_e32 v[120:121], s[14:15]
	v_mov_b64_e32 v[112:113], s[14:15]
	s_waitcnt lgkmcnt(9)
	v_mov_b32_e32 v24, v56
	v_mov_b32_e32 v25, v57
	v_mov_b64_e32 v[98:99], s[12:13]
	v_mov_b64_e32 v[170:171], s[12:13]
	v_mov_b32_e32 v18, v64
	v_mov_b32_e32 v19, v65
	v_mov_b64_e32 v[166:167], s[12:13]
	v_mov_b64_e32 v[154:155], s[12:13]
	v_mov_b64_e32 v[150:151], s[12:13]
	v_mov_b64_e32 v[142:143], s[12:13]
	v_mov_b64_e32 v[134:135], s[12:13]
	v_mov_b64_e32 v[118:119], s[12:13]
	v_mov_b64_e32 v[110:111], s[12:13]
	s_waitcnt lgkmcnt(6)
	v_mov_b32_e32 v48, v76
	v_mov_b32_e32 v49, v77
	s_nop 1
	v_mfma_scale_f32_16x16x128_f8f6f4 v[170:173], v[20:25], v[44:49], v[170:173], v58, v78 op_sel_hi:[0,0,0] cbsz:2 blgp:2
	s_nop 1
	v_mfma_scale_f32_16x16x128_f8f6f4 v[166:169], v[14:19], v[44:49], v[166:169], v66, v78 op_sel_hi:[0,0,0] cbsz:2 blgp:2
	s_waitcnt lgkmcnt(4)
	v_mov_b32_e32 v42, v72
	v_mov_b32_e32 v43, v73
	s_nop 1
	v_mfma_scale_f32_16x16x128_f8f6f4 v[154:157], v[20:25], v[38:43], v[154:157], v58, v74 op_sel_hi:[0,0,0] cbsz:2 blgp:2
	s_nop 1
	v_mfma_scale_f32_16x16x128_f8f6f4 v[150:153], v[14:19], v[38:43], v[150:153], v66, v74 op_sel_hi:[0,0,0] cbsz:2 blgp:2
	s_waitcnt lgkmcnt(2)
	v_mov_b32_e32 v36, v68
	v_mov_b32_e32 v37, v69
	s_nop 1
	v_mfma_scale_f32_16x16x128_f8f6f4 v[142:145], v[20:25], v[32:37], v[142:145], v58, v70 op_sel_hi:[0,0,0] cbsz:2 blgp:2
	s_nop 1
	v_mfma_scale_f32_16x16x128_f8f6f4 v[134:137], v[14:19], v[32:37], v[134:137], v66, v70 op_sel_hi:[0,0,0] cbsz:2 blgp:2
	s_waitcnt lgkmcnt(0)
	v_mov_b32_e32 v30, v60
	v_mov_b32_e32 v31, v61
	s_nop 1
	v_mfma_scale_f32_16x16x128_f8f6f4 v[118:121], v[20:25], v[26:31], v[118:121], v58, v62 op_sel_hi:[0,0,0] cbsz:2 blgp:2
	s_nop 1
	v_mfma_scale_f32_16x16x128_f8f6f4 v[110:113], v[14:19], v[26:31], v[110:113], v66, v62 op_sel_hi:[0,0,0] cbsz:2 blgp:2
	s_setprio 1
	s_setprio 0
	v_mov_b64_e32 v[180:181], s[14:15]
	v_mov_b64_e32 v[176:177], s[14:15]
	v_mov_b64_e32 v[164:165], s[14:15]
	v_mov_b64_e32 v[160:161], s[14:15]
	v_mov_b64_e32 v[148:149], s[14:15]
	v_mov_b64_e32 v[140:141], s[14:15]
	v_mov_b64_e32 v[128:129], s[14:15]
	v_mov_b32_e32 v12, v186
	v_mov_b32_e32 v13, v187
	v_mov_b64_e32 v[178:179], s[12:13]
	v_mov_b32_e32 v6, v182
	v_mov_b32_e32 v7, v183
	v_mov_b64_e32 v[174:175], s[12:13]
	v_mov_b64_e32 v[162:163], s[12:13]
	v_mov_b64_e32 v[158:159], s[12:13]
	v_mov_b64_e32 v[146:147], s[12:13]
	v_mov_b64_e32 v[138:139], s[12:13]
	v_mov_b64_e32 v[126:127], s[12:13]
	s_nop 1
	v_mfma_scale_f32_16x16x128_f8f6f4 v[178:181], v[8:13], v[44:49], v[178:181], v188, v78 op_sel_hi:[0,0,0] cbsz:2 blgp:2
	s_nop 1
	v_mfma_scale_f32_16x16x128_f8f6f4 v[174:177], v[2:7], v[44:49], v[174:177], v184, v78 op_sel_hi:[0,0,0] cbsz:2 blgp:2
	s_nop 1
	v_mfma_scale_f32_16x16x128_f8f6f4 v[162:165], v[8:13], v[38:43], v[162:165], v188, v74 op_sel_hi:[0,0,0] cbsz:2 blgp:2
	s_nop 1
	v_mfma_scale_f32_16x16x128_f8f6f4 v[158:161], v[2:7], v[38:43], v[158:161], v184, v74 op_sel_hi:[0,0,0] cbsz:2 blgp:2
	s_nop 1
	v_mfma_scale_f32_16x16x128_f8f6f4 v[146:149], v[8:13], v[32:37], v[146:149], v188, v70 op_sel_hi:[0,0,0] cbsz:2 blgp:2
	s_nop 1
	v_mfma_scale_f32_16x16x128_f8f6f4 v[138:141], v[2:7], v[32:37], v[138:141], v184, v70 op_sel_hi:[0,0,0] cbsz:2 blgp:2
	s_nop 1
	v_mfma_scale_f32_16x16x128_f8f6f4 v[126:129], v[8:13], v[26:31], v[126:129], v188, v62 op_sel_hi:[0,0,0] cbsz:2 blgp:2
	s_nop 1
	v_mfma_scale_f32_16x16x128_f8f6f4 v[98:101], v[2:7], v[26:31], v[98:101], v184, v62 op_sel_hi:[0,0,0] cbsz:2 blgp:2
	s_setprio 1
	s_barrier
	ds_read_b128 v[44:47], v224 offset:16384
	ds_read_b128 v[80:83], v224 offset:17408
	ds_read_b128 v[38:41], v224 offset:18432
	ds_read_b128 v[72:75], v224 offset:19456
	ds_read_b128 v[32:35], v224 offset:20480
	ds_read_b128 v[194:197], v224 offset:21504
	ds_read_b128 v[26:29], v224 offset:22528
	ds_read_b128 v[190:193], v224 offset:23552
	s_mov_b32 s41, m0
	s_mov_b32 m0, s47
	s_nop 0
	global_load_lds_dwordx4 v217, s[18:19]
	s_mov_b32 m0, s41
	s_nop 0
	s_mov_b32 s41, m0
	s_mov_b32 m0, s66
	s_nop 0
	global_load_lds_dwordx4 v218, s[18:19]
	s_mov_b32 m0, s41
	s_add_u32 s18, s48, 0x40100
	s_addc_u32 s19, s49, 0
	s_mov_b32 s41, m0
	s_mov_b32 m0, s67
	s_nop 0
	global_load_lds_dwordx4 v217, s[18:19]
	s_mov_b32 m0, s41
	s_and_b64 vcc, exec, s[16:17]
	s_mov_b32 s41, m0
	s_mov_b32 m0, s68
	s_nop 0
	global_load_lds_dwordx4 v218, s[18:19]
	s_mov_b32 m0, s41
	s_mov_b32 s18, m0
	s_mov_b32 m0, s35
	s_nop 0
	global_load_lds_dwordx4 v50, s[24:25]
	s_mov_b32 m0, s18
	s_nop 0
	s_mov_b32 s18, m0
	s_mov_b32 m0, s69
	s_nop 0
	global_load_lds_dwordx4 v51, s[24:25]
	s_mov_b32 m0, s18
	s_cbranch_vccz .LBB0_1148
	s_waitcnt vmcnt(16)
	s_cbranch_execnz .LBB0_1134

; #define LAS __attribute__((address_space(3)))
; #define PG8_STAGEB(bufoff, gbase) PG8_STAGE2(bufoff, gbase, voffB[0], voffB[1])
; #define PG8_STAGEA(bufoff, gbase, h) PG8_STAGE2(bufoff, gbase, voffA[h][0], voffA[h][1])
; #define PG8_STAGEAS(bufoff, gbase, h) PG8_STAGE2(bufoff, gbase, voffA[h][0], voffA[h][1])
; #define PG8_LDA(dst, b, h) do { _Pragma("unroll") for (int m = 0; m < 4; ++m) _Pragma("unroll") for (int k = 0; k < 2; ++k) dst[m][k] = *(const LAS bf16x8*)(lds + PG8_SA(b, h) + aoff + m * 2048 + k * 1024); } while (0)
; #define PG8_LDB(dst, b, h) do { _Pragma("unroll") for (int n = 0; n < 2; ++n) _Pragma("unroll") for (int k = 0; k < 2; ++k) dst[n][k] = *(const LAS bf16x8*)(lds + PG8_SB(b, h) + boff + n * 2048 + k * 1024); } while (0)
; #define PG8_WAIT_K0() do { if (EST > 0 && t == 0 && ui > 0) asm volatile("s_waitcnt vmcnt(%0)" :: "n"((HM ? 6 : 8) + EST) : "memory"); else PG8_WAIT_K(); } while (0)
; #define PG8_WAIT_L(n) asm volatile("s_waitcnt lgkmcnt(" #n ")" ::: "memory")
; #define PG8_BAR __builtin_amdgcn_s_barrier()
; #define PG8_SCHED __builtin_amdgcn_sched_barrier(0)
;     ...
;             PG8_LDB(B0, 0, 0); PG8_LDB(B1, 0, 1); PG8_SCHED; PG8_LDA(At, 0, 0); if constexpr (!HM) PG8_STAGEA(PG8_SA(1, 1), a1, 1);
;             if constexpr (Sched::kGather) { if (last && has_next) { const u32x4 tn = *(const LAS u32x4*)(S.aux + tid * 16); voffA[0][0] = tn.x; voffA[0][1] = tn.y; voffA[1][0] = tn.z; voffA[1][1] = tn.w; } }
;             PG8_WAIT_K0(); PG8_WAIT_L(0); PG8_BAR; PG8_MMA(0, 0, At, B0); PG8_MMA(0, 1, At, B1); PG8_BAR; PG8_SCHED;
;             if constexpr (!HM) PG8_LDA(At, 0, 1);
;             PG8_STAGEB(PG8_SB(0, 0), b2); PG8_STAGEB(PG8_SB(0, 1), b2 + hstepB); PG8_STAGEAS(PG8_SA(0, 0), a2, 0);
;             PG8_WAIT_K0(); PG8_WAIT_L(0); PG8_BAR; if constexpr (!HM) { PG8_MMA(1, 0, At, B0); PG8_MMA(1, 1, At, B1); } PG8_BAR; PG8_SCHED;
;             PG8_LDB(B0, 1, 0); PG8_LDB(B1, 1, 1); PG8_SCHED; PG8_LDA(At, 1, 0); if constexpr (!HM) PG8_STAGEAS(PG8_SA(0, 1), a2, 1);
.LBB0_1134:
	s_waitcnt lgkmcnt(0)
	s_add_u32 s50, s48, 0x180
	s_addc_u32 s51, s49, 0
	s_barrier
	s_setprio 0
	s_mov_b32 s16, 0
	s_mov_b32 s18, s16
	s_mov_b32 s19, s16
	s_waitcnt lgkmcnt(6)
	v_mov_b32_e32 v48, v80
	v_mov_b32_e32 v49, v81
	s_mov_b32 s17, s16
	v_mov_b64_e32 v[116:117], s[18:19]
	v_mov_b64_e32 v[108:109], s[18:19]
	s_waitcnt lgkmcnt(4)
	v_mov_b32_e32 v42, v72
	v_mov_b32_e32 v43, v73
	v_mov_b64_e32 v[96:97], s[18:19]
	v_mov_b64_e32 v[88:89], s[18:19]
	v_mov_b64_e32 v[80:81], s[18:19]
	v_mov_b64_e32 v[72:73], s[18:19]
	v_mov_b64_e32 v[64:65], s[18:19]
	v_mov_b64_e32 v[114:115], s[16:17]
	v_mov_b64_e32 v[106:107], s[16:17]
	v_mov_b64_e32 v[94:95], s[16:17]
	v_mov_b64_e32 v[86:87], s[16:17]
	v_mov_b64_e32 v[78:79], s[16:17]
	v_mov_b64_e32 v[70:71], s[16:17]
	v_mov_b64_e32 v[62:63], s[16:17]
	v_mov_b64_e32 v[56:57], s[18:19]
	s_nop 1
	v_mfma_scale_f32_16x16x128_f8f6f4 v[114:117], v[20:25], v[44:49], v[114:117], v58, v82 op_sel_hi:[0,0,0] cbsz:2 blgp:2
	s_nop 1
	v_mfma_scale_f32_16x16x128_f8f6f4 v[106:109], v[14:19], v[44:49], v[106:109], v66, v82 op_sel_hi:[0,0,0] cbsz:2 blgp:2
	s_nop 1
	v_mfma_scale_f32_16x16x128_f8f6f4 v[94:97], v[20:25], v[38:43], v[94:97], v58, v74 op_sel_hi:[0,0,0] cbsz:2 blgp:2
	s_nop 1
	v_mfma_scale_f32_16x16x128_f8f6f4 v[86:89], v[14:19], v[38:43], v[86:89], v66, v74 op_sel_hi:[0,0,0] cbsz:2 blgp:2
	s_waitcnt lgkmcnt(2)
	v_mov_b32_e32 v36, v194
	v_mov_b32_e32 v37, v195
	s_nop 1
	v_mfma_scale_f32_16x16x128_f8f6f4 v[78:81], v[20:25], v[32:37], v[78:81], v58, v196 op_sel_hi:[0,0,0] cbsz:2 blgp:2
	s_nop 1
	v_mfma_scale_f32_16x16x128_f8f6f4 v[70:73], v[14:19], v[32:37], v[70:73], v66, v196 op_sel_hi:[0,0,0] cbsz:2 blgp:2
	s_waitcnt lgkmcnt(0)
	v_mov_b32_e32 v30, v190
	v_mov_b32_e32 v31, v191
	s_nop 1
	v_mfma_scale_f32_16x16x128_f8f6f4 v[62:65], v[20:25], v[26:31], v[62:65], v58, v192 op_sel_hi:[0,0,0] cbsz:2 blgp:2
	v_mov_b64_e32 v[60:61], s[18:19]
	v_mov_b64_e32 v[54:55], s[16:17]
	v_mov_b64_e32 v[58:59], s[16:17]
	s_nop 1
	v_mfma_scale_f32_16x16x128_f8f6f4 v[58:61], v[14:19], v[26:31], v[58:61], v66, v192 op_sel_hi:[0,0,0] cbsz:2 blgp:2
	s_setprio 1
	s_setprio 0
	v_mov_b64_e32 v[132:133], s[18:19]
	v_mov_b64_e32 v[124:125], s[18:19]
	v_mov_b64_e32 v[104:105], s[18:19]
	v_mov_b64_e32 v[92:93], s[18:19]
	v_mov_b64_e32 v[130:131], s[16:17]
	v_mov_b64_e32 v[122:123], s[16:17]
	v_mov_b64_e32 v[102:103], s[16:17]
	v_mov_b64_e32 v[90:91], s[16:17]
	s_nop 1
	v_mfma_scale_f32_16x16x128_f8f6f4 v[130:133], v[8:13], v[44:49], v[130:133], v188, v82 op_sel_hi:[0,0,0] cbsz:2 blgp:2
	s_nop 1
	v_mfma_scale_f32_16x16x128_f8f6f4 v[122:125], v[2:7], v[44:49], v[122:125], v184, v82 op_sel_hi:[0,0,0] cbsz:2 blgp:2
	s_nop 1
	v_mfma_scale_f32_16x16x128_f8f6f4 v[102:105], v[8:13], v[38:43], v[102:105], v188, v74 op_sel_hi:[0,0,0] cbsz:2 blgp:2
	s_nop 1
	v_mfma_scale_f32_16x16x128_f8f6f4 v[90:93], v[2:7], v[38:43], v[90:93], v184, v74 op_sel_hi:[0,0,0] cbsz:2 blgp:2
	v_mov_b64_e32 v[84:85], s[18:19]
	v_mov_b64_e32 v[76:77], s[18:19]
	v_mov_b64_e32 v[68:69], s[18:19]
	v_mov_b64_e32 v[82:83], s[16:17]
	v_mov_b64_e32 v[74:75], s[16:17]
	v_mov_b64_e32 v[66:67], s[16:17]
	s_nop 1
	v_mfma_scale_f32_16x16x128_f8f6f4 v[82:85], v[8:13], v[32:37], v[82:85], v188, v196 op_sel_hi:[0,0,0] cbsz:2 blgp:2
	s_nop 1
	v_mfma_scale_f32_16x16x128_f8f6f4 v[74:77], v[2:7], v[32:37], v[74:77], v184, v196 op_sel_hi:[0,0,0] cbsz:2 blgp:2
	s_nop 1
	v_mfma_scale_f32_16x16x128_f8f6f4 v[66:69], v[8:13], v[26:31], v[66:69], v188, v192 op_sel_hi:[0,0,0] cbsz:2 blgp:2
	s_nop 1
	v_mfma_scale_f32_16x16x128_f8f6f4 v[54:57], v[2:7], v[26:31], v[54:57], v184, v192 op_sel_hi:[0,0,0] cbsz:2 blgp:2
	s_setprio 1
	s_barrier
	v_add_u32_e32 v232, 0x18000, v223
	v_add_u32_e32 v233, 0x1c000, v223
	ds_read_b128 v[20:23], v232
	ds_read_b128 v[38:41], v232 offset:1024
	ds_read_b128 v[14:17], v232 offset:2048
	ds_read_b128 v[34:37], v232 offset:3072
	ds_read_b128 v[8:11], v233
	ds_read_b128 v[30:33], v233 offset:1024
	ds_read_b128 v[2:5], v233 offset:2048
	ds_read_b128 v[26:29], v233 offset:3072
	ds_read_b128 v[42:45], v224 offset:32768
	ds_read_b128 v[46:49], v224 offset:33792
	ds_read_b128 v[182:185], v224 offset:34816
	ds_read_b128 v[198:201], v224 offset:35840
	ds_read_b128 v[188:191], v224 offset:36864
	ds_read_b128 v[202:205], v224 offset:37888
	ds_read_b128 v[194:197], v224 offset:38912
	ds_read_b128 v[206:209], v224 offset:39936
	s_mov_b32 s17, m0
	s_mov_b32 m0, s70
	s_nop 0
	global_load_lds_dwordx4 v52, s[24:25]
	s_mov_b32 m0, s17
	s_nop 0
	s_mov_b32 s17, m0
	s_mov_b32 m0, s71
	s_nop 0
	global_load_lds_dwordx4 v53, s[24:25]
	s_mov_b32 m0, s17
	s_waitcnt vmcnt(8)
	s_waitcnt lgkmcnt(0)
	s_barrier
; #define PG8_STAGEB(bufoff, gbase) PG8_STAGE2(bufoff, gbase, voffB[0], voffB[1])
; #define PG8_STAGEAS(bufoff, gbase, h) PG8_STAGE2(bufoff, gbase, voffA[h][0], voffA[h][1])
; #define PG8_LDA(dst, b, h) do { _Pragma("unroll") for (int m = 0; m < 4; ++m) _Pragma("unroll") for (int k = 0; k < 2; ++k) dst[m][k] = *(const LAS bf16x8*)(lds + PG8_SA(b, h) + aoff + m * 2048 + k * 1024); } while (0)
; #define PG8_LDB(dst, b, h) do { _Pragma("unroll") for (int n = 0; n < 2; ++n) _Pragma("unroll") for (int k = 0; k < 2; ++k) dst[n][k] = *(const LAS bf16x8*)(lds + PG8_SB(b, h) + boff + n * 2048 + k * 1024); } while (0)
; #define PG8_WAIT_K() do { if constexpr (HM) PG8_WAIT_V(6); else PG8_WAIT_V(8); } while (0)
; #define PG8_WAIT_K0() do { if (EST > 0 && t == 0 && ui > 0) asm volatile("s_waitcnt vmcnt(%0)" :: "n"((HM ? 6 : 8) + EST) : "memory"); else PG8_WAIT_K(); } while (0)
; #define PG8_WAIT_L(n) asm volatile("s_waitcnt lgkmcnt(" #n ")" ::: "memory")
; #define PG8_BAR __builtin_amdgcn_s_barrier()
; #define PG8_SCHED __builtin_amdgcn_sched_barrier(0)
;     ...
;             PG8_WAIT_K0(); PG8_WAIT_L(0); PG8_BAR; if constexpr (!HM) { PG8_MMA(1, 0, At, B0); PG8_MMA(1, 1, At, B1); } PG8_BAR; PG8_SCHED;
;             PG8_LDB(B0, 1, 0); PG8_LDB(B1, 1, 1); PG8_SCHED; PG8_LDA(At, 1, 0); if constexpr (!HM) PG8_STAGEAS(PG8_SA(0, 1), a2, 1);
;             PG8_WAIT_K(); PG8_WAIT_L(0); PG8_BAR; PG8_MMA(0, 0, At, B0); PG8_MMA(0, 1, At, B1); PG8_BAR; PG8_SCHED;
;             if constexpr (!HM) PG8_LDA(At, 1, 1);
;             PG8_STAGEB(PG8_SB(1, 0), b3); PG8_STAGEB(PG8_SB(1, 1), b3 + hstepB); PG8_STAGEAS(PG8_SA(1, 0), a3, 0);
;             PG8_WAIT_K(); PG8_WAIT_L(0); PG8_BAR; if constexpr (!HM) { PG8_MMA(1, 0, At, B0); PG8_MMA(1, 1, At, B1); } PG8_BAR; PG8_SCHED;
	s_setprio 0
	s_waitcnt lgkmcnt(14)
	v_mov_b32_e32 v24, v38
	v_mov_b32_e32 v25, v39
	s_waitcnt lgkmcnt(6)
	s_nop 1
	v_mfma_scale_f32_16x16x128_f8f6f4 v[170:173], v[20:25], v[42:47], v[170:173], v40, v48 op_sel_hi:[0,0,0] cbsz:2 blgp:2
	v_mov_b32_e32 v18, v34
	v_mov_b32_e32 v19, v35
	s_nop 1
	v_mfma_scale_f32_16x16x128_f8f6f4 v[166:169], v[14:19], v[42:47], v[166:169], v36, v48 op_sel_hi:[0,0,0] cbsz:2 blgp:2
	s_waitcnt lgkmcnt(4)
	v_mov_b32_e32 v186, v198
	v_mov_b32_e32 v187, v199
	s_nop 1
	v_mfma_scale_f32_16x16x128_f8f6f4 v[154:157], v[20:25], v[182:187], v[154:157], v40, v200 op_sel_hi:[0,0,0] cbsz:2 blgp:2
	s_nop 1
	v_mfma_scale_f32_16x16x128_f8f6f4 v[150:153], v[14:19], v[182:187], v[150:153], v36, v200 op_sel_hi:[0,0,0] cbsz:2 blgp:2
	s_waitcnt lgkmcnt(2)
	v_mov_b32_e32 v192, v202
	v_mov_b32_e32 v193, v203
	s_nop 1
	v_mfma_scale_f32_16x16x128_f8f6f4 v[142:145], v[20:25], v[188:193], v[142:145], v40, v204 op_sel_hi:[0,0,0] cbsz:2 blgp:2
	s_nop 1
	v_mfma_scale_f32_16x16x128_f8f6f4 v[134:137], v[14:19], v[188:193], v[134:137], v36, v204 op_sel_hi:[0,0,0] cbsz:2 blgp:2
	s_waitcnt lgkmcnt(0)
	v_mov_b32_e32 v198, v206
	v_mov_b32_e32 v199, v207
	s_nop 1
	v_mfma_scale_f32_16x16x128_f8f6f4 v[118:121], v[20:25], v[194:199], v[118:121], v40, v208 op_sel_hi:[0,0,0] cbsz:2 blgp:2
	s_nop 1
	v_mfma_scale_f32_16x16x128_f8f6f4 v[110:113], v[14:19], v[194:199], v[110:113], v36, v208 op_sel_hi:[0,0,0] cbsz:2 blgp:2
	s_setprio 1
	s_setprio 0
	v_mov_b32_e32 v12, v30
	v_mov_b32_e32 v13, v31
	s_nop 1
	v_mfma_scale_f32_16x16x128_f8f6f4 v[178:181], v[8:13], v[42:47], v[178:181], v32, v48 op_sel_hi:[0,0,0] cbsz:2 blgp:2
	v_mov_b32_e32 v6, v26
	v_mov_b32_e32 v7, v27
	s_nop 1
	v_mfma_scale_f32_16x16x128_f8f6f4 v[174:177], v[2:7], v[42:47], v[174:177], v28, v48 op_sel_hi:[0,0,0] cbsz:2 blgp:2
	s_nop 1
	v_mfma_scale_f32_16x16x128_f8f6f4 v[162:165], v[8:13], v[182:187], v[162:165], v32, v200 op_sel_hi:[0,0,0] cbsz:2 blgp:2
	s_nop 1
	v_mfma_scale_f32_16x16x128_f8f6f4 v[158:161], v[2:7], v[182:187], v[158:161], v28, v200 op_sel_hi:[0,0,0] cbsz:2 blgp:2
	s_nop 1
	v_mfma_scale_f32_16x16x128_f8f6f4 v[146:149], v[8:13], v[188:193], v[146:149], v32, v204 op_sel_hi:[0,0,0] cbsz:2 blgp:2
	s_nop 1
	v_mfma_scale_f32_16x16x128_f8f6f4 v[138:141], v[2:7], v[188:193], v[138:141], v28, v204 op_sel_hi:[0,0,0] cbsz:2 blgp:2
	s_nop 1
	v_mfma_scale_f32_16x16x128_f8f6f4 v[126:129], v[8:13], v[194:199], v[126:129], v32, v208 op_sel_hi:[0,0,0] cbsz:2 blgp:2
	s_nop 1
	v_mfma_scale_f32_16x16x128_f8f6f4 v[98:101], v[2:7], v[194:199], v[98:101], v28, v208 op_sel_hi:[0,0,0] cbsz:2 blgp:2
	s_setprio 1
	s_barrier
	ds_read_b128 v[42:45], v224 offset:49152
	ds_read_b128 v[46:49], v224 offset:50176
	ds_read_b128 v[182:185], v224 offset:51200
	ds_read_b128 v[198:201], v224 offset:52224
	ds_read_b128 v[188:191], v224 offset:53248
	ds_read_b128 v[202:205], v224 offset:54272
	ds_read_b128 v[194:197], v224 offset:55296
	ds_read_b128 v[206:209], v224 offset:56320
	s_mov_b32 s17, m0
	s_mov_b32 m0, s72
	s_nop 0
	global_load_lds_dwordx4 v217, s[50:51]
	s_mov_b32 m0, s17
	s_add_u32 s18, s48, 0x40180
	s_mov_b32 s17, m0
	s_mov_b32 m0, s73
	s_nop 0
	global_load_lds_dwordx4 v218, s[50:51]
	s_mov_b32 m0, s17
	s_addc_u32 s19, s49, 0
	s_mov_b32 s17, m0
	s_mov_b32 m0, s76
	s_nop 0
	global_load_lds_dwordx4 v217, s[18:19]
	s_mov_b32 m0, s17
	s_nop 0
	s_mov_b32 s17, m0
	s_mov_b32 m0, s77
	s_nop 0
	global_load_lds_dwordx4 v218, s[18:19]
	s_mov_b32 m0, s17
	s_nop 0
	s_mov_b32 s17, m0
	s_mov_b32 m0, s74
	s_nop 0
	global_load_lds_dwordx4 v50, s[26:27]
	s_mov_b32 m0, s17
	s_nop 0
	s_mov_b32 s17, m0
	s_mov_b32 m0, s75
	s_nop 0
	global_load_lds_dwordx4 v51, s[26:27]
	s_mov_b32 m0, s17
	s_waitcnt vmcnt(8)
	s_waitcnt lgkmcnt(0)
	s_barrier
	s_setprio 0
	s_waitcnt lgkmcnt(6)
	s_nop 1
	v_mfma_scale_f32_16x16x128_f8f6f4 v[114:117], v[20:25], v[42:47], v[114:117], v40, v48 op_sel_hi:[0,0,0] cbsz:2 blgp:2
	s_nop 1
	v_mfma_scale_f32_16x16x128_f8f6f4 v[106:109], v[14:19], v[42:47], v[106:109], v36, v48 op_sel_hi:[0,0,0] cbsz:2 blgp:2
	s_waitcnt lgkmcnt(4)
	v_mov_b32_e32 v186, v198
	v_mov_b32_e32 v187, v199
	s_nop 1
	v_mfma_scale_f32_16x16x128_f8f6f4 v[94:97], v[20:25], v[182:187], v[94:97], v40, v200 op_sel_hi:[0,0,0] cbsz:2 blgp:2
	s_nop 1
	v_mfma_scale_f32_16x16x128_f8f6f4 v[86:89], v[14:19], v[182:187], v[86:89], v36, v200 op_sel_hi:[0,0,0] cbsz:2 blgp:2
	s_waitcnt lgkmcnt(2)
	v_mov_b32_e32 v192, v202
	v_mov_b32_e32 v193, v203
	s_nop 1
	v_mfma_scale_f32_16x16x128_f8f6f4 v[78:81], v[20:25], v[188:193], v[78:81], v40, v204 op_sel_hi:[0,0,0] cbsz:2 blgp:2
	s_nop 1
	v_mfma_scale_f32_16x16x128_f8f6f4 v[70:73], v[14:19], v[188:193], v[70:73], v36, v204 op_sel_hi:[0,0,0] cbsz:2 blgp:2
	s_waitcnt lgkmcnt(0)
	v_mov_b32_e32 v198, v206
	v_mov_b32_e32 v199, v207
	s_nop 1
	v_mfma_scale_f32_16x16x128_f8f6f4 v[62:65], v[20:25], v[194:199], v[62:65], v40, v208 op_sel_hi:[0,0,0] cbsz:2 blgp:2
	s_nop 1
	v_mfma_scale_f32_16x16x128_f8f6f4 v[58:61], v[14:19], v[194:199], v[58:61], v36, v208 op_sel_hi:[0,0,0] cbsz:2 blgp:2
	s_setprio 1
	s_setprio 0
	s_nop 1
	v_mfma_scale_f32_16x16x128_f8f6f4 v[130:133], v[8:13], v[42:47], v[130:133], v32, v48 op_sel_hi:[0,0,0] cbsz:2 blgp:2
	s_nop 1
	v_mfma_scale_f32_16x16x128_f8f6f4 v[122:125], v[2:7], v[42:47], v[122:125], v28, v48 op_sel_hi:[0,0,0] cbsz:2 blgp:2
	s_nop 1
	v_mfma_scale_f32_16x16x128_f8f6f4 v[102:105], v[8:13], v[182:187], v[102:105], v32, v200 op_sel_hi:[0,0,0] cbsz:2 blgp:2
	s_nop 1
	v_mfma_scale_f32_16x16x128_f8f6f4 v[90:93], v[2:7], v[182:187], v[90:93], v28, v200 op_sel_hi:[0,0,0] cbsz:2 blgp:2
	s_nop 1
	v_mfma_scale_f32_16x16x128_f8f6f4 v[82:85], v[8:13], v[188:193], v[82:85], v32, v204 op_sel_hi:[0,0,0] cbsz:2 blgp:2
	s_nop 1
	v_mfma_scale_f32_16x16x128_f8f6f4 v[74:77], v[2:7], v[188:193], v[74:77], v28, v204 op_sel_hi:[0,0,0] cbsz:2 blgp:2
	s_nop 1
	v_mfma_scale_f32_16x16x128_f8f6f4 v[66:69], v[8:13], v[194:199], v[66:69], v32, v208 op_sel_hi:[0,0,0] cbsz:2 blgp:2
	s_nop 1
	v_mfma_scale_f32_16x16x128_f8f6f4 v[54:57], v[2:7], v[194:199], v[54:57], v28, v208 op_sel_hi:[0,0,0] cbsz:2 blgp:2
	s_setprio 1
	s_barrier
	s_mov_b64 s[18:19], 0x200
	s_xor_b64 s[50:51], s[10:11], -1
	s_branch .LBB0_1136
; #define LAS __attribute__((address_space(3)))
; #define PG8_STAGEB(bufoff, gbase) PG8_STAGE2(bufoff, gbase, voffB[0], voffB[1])
; #define PG8_STAGEA(bufoff, gbase, h) PG8_STAGE2(bufoff, gbase, voffA[h][0], voffA[h][1])
; #define PG8_STAGEAS(bufoff, gbase, h) PG8_STAGE2(bufoff, gbase, voffA[h][0], voffA[h][1])
; #define PG8_LDA(dst, b, h) do { _Pragma("unroll") for (int m = 0; m < 4; ++m) _Pragma("unroll") for (int k = 0; k < 2; ++k) dst[m][k] = *(const LAS bf16x8*)(lds + PG8_SA(b, h) + aoff + m * 2048 + k * 1024); } while (0)
; #define PG8_LDB(dst, b, h) do { _Pragma("unroll") for (int n = 0; n < 2; ++n) _Pragma("unroll") for (int k = 0; k < 2; ++k) dst[n][k] = *(const LAS bf16x8*)(lds + PG8_SB(b, h) + boff + n * 2048 + k * 1024); } while (0)
;     ...
;             const char* a1 = cA + (size_t)(t + 1) * kstep;
;             const char* a2 = last ? nA : cA + (size_t)(t + 2) * kstep; const char* b2 = last ? nB : cB + (size_t)(t + 2) * kstep;
;             const char* a3 = a2 + kstep; const char* b3 = b2 + kstep;
;             PG8_LDB(B0, 0, 0); PG8_LDB(B1, 0, 1); PG8_SCHED; PG8_LDA(At, 0, 0); if constexpr (!HM) PG8_STAGEA(PG8_SA(1, 1), a1, 1);
;             if constexpr (Sched::kGather) { if (last && has_next) { const u32x4 tn = *(const LAS u32x4*)(S.aux + tid * 16); voffA[0][0] = tn.x; voffA[0][1] = tn.y; voffA[1][0] = tn.z; voffA[1][1] = tn.w; } }
;             PG8_WAIT_K0(); PG8_WAIT_L(0); PG8_BAR; PG8_MMA(0, 0, At, B0); PG8_MMA(0, 1, At, B1); PG8_BAR; PG8_SCHED;
;             if constexpr (!HM) PG8_LDA(At, 0, 1);
;             PG8_STAGEB(PG8_SB(0, 0), b2); PG8_STAGEB(PG8_SB(0, 1), b2 + hstepB); PG8_STAGEAS(PG8_SA(0, 0), a2, 0);
;             PG8_WAIT_K0(); PG8_WAIT_L(0); PG8_BAR; if constexpr (!HM) { PG8_MMA(1, 0, At, B0); PG8_MMA(1, 1, At, B1); } PG8_BAR; PG8_SCHED;
;             PG8_LDB(B0, 1, 0); PG8_LDB(B1, 1, 1); PG8_SCHED; PG8_LDA(At, 1, 0); if constexpr (!HM) PG8_STAGEAS(PG8_SA(0, 1), a2, 1);
;             PG8_WAIT_K(); PG8_WAIT_L(0); PG8_BAR; PG8_MMA(0, 0, At, B0); PG8_MMA(0, 1, At, B1); PG8_BAR; PG8_SCHED;
;             if constexpr (!HM) PG8_LDA(At, 1, 1);
;             PG8_STAGEB(PG8_SB(1, 0), b3); PG8_STAGEB(PG8_SB(1, 1), b3 + hstepB); PG8_STAGEAS(PG8_SA(1, 0), a3, 0);
;             PG8_WAIT_K(); PG8_WAIT_L(0); PG8_BAR; if constexpr (!HM) { PG8_MMA(1, 0, At, B0); PG8_MMA(1, 1, At, B1); } PG8_BAR; PG8_SCHED;
.LBB0_1135:
	s_and_b64 s[52:53], s[54:55], exec
	s_cselect_b32 s41, 0, s18
	s_cselect_b32 s17, 0, s19
	s_add_u32 s58, s0, s41
	s_addc_u32 s59, s1, s17
	s_add_u32 s17, s48, s18
	s_addc_u32 s41, s49, s19
	s_add_u32 s52, s58, 0x80
	s_addc_u32 s53, s59, 0
	s_waitcnt vmcnt(8)
	s_and_b64 s[54:55], s[54:55], exec
	s_waitcnt lgkmcnt(0)
	s_cselect_b32 s54, s44, s17
	s_cselect_b32 s55, s45, s41
	s_add_u32 s56, s54, 0x80
	s_addc_u32 s57, s55, 0
	s_barrier
	s_setprio 0
	s_waitcnt lgkmcnt(6)
	v_mov_b32_e32 v48, v210
	v_mov_b32_e32 v49, v211
	v_mov_b32_e32 v24, v194
	v_mov_b32_e32 v25, v195
	s_nop 1
	v_mfma_scale_f32_16x16x128_f8f6f4 v[170:173], v[20:25], v[44:49], v[170:173], v196, v212 op_sel_hi:[0,0,0] cbsz:2 blgp:2
	v_mov_b32_e32 v18, v190
	v_mov_b32_e32 v19, v191
	s_nop 1
	v_mfma_scale_f32_16x16x128_f8f6f4 v[166:169], v[14:19], v[44:49], v[166:169], v192, v212 op_sel_hi:[0,0,0] cbsz:2 blgp:2
	s_waitcnt lgkmcnt(4)
	v_mov_b32_e32 v42, v206
	v_mov_b32_e32 v43, v207
	s_nop 1
	v_mfma_scale_f32_16x16x128_f8f6f4 v[154:157], v[20:25], v[38:43], v[154:157], v196, v208 op_sel_hi:[0,0,0] cbsz:2 blgp:2
	s_nop 1
	v_mfma_scale_f32_16x16x128_f8f6f4 v[150:153], v[14:19], v[38:43], v[150:153], v192, v208 op_sel_hi:[0,0,0] cbsz:2 blgp:2
	s_waitcnt lgkmcnt(2)
	v_mov_b32_e32 v36, v202
	v_mov_b32_e32 v37, v203
	s_nop 1
	v_mfma_scale_f32_16x16x128_f8f6f4 v[142:145], v[20:25], v[32:37], v[142:145], v196, v204 op_sel_hi:[0,0,0] cbsz:2 blgp:2
	s_nop 1
	v_mfma_scale_f32_16x16x128_f8f6f4 v[134:137], v[14:19], v[32:37], v[134:137], v192, v204 op_sel_hi:[0,0,0] cbsz:2 blgp:2
	s_waitcnt lgkmcnt(0)
	v_mov_b32_e32 v30, v198
	v_mov_b32_e32 v31, v199
	s_nop 1
	v_mfma_scale_f32_16x16x128_f8f6f4 v[118:121], v[20:25], v[26:31], v[118:121], v196, v200 op_sel_hi:[0,0,0] cbsz:2 blgp:2
	s_nop 1
	v_mfma_scale_f32_16x16x128_f8f6f4 v[110:113], v[14:19], v[26:31], v[110:113], v192, v200 op_sel_hi:[0,0,0] cbsz:2 blgp:2
	s_setprio 1
	s_setprio 0
	v_mov_b32_e32 v12, v182
	v_mov_b32_e32 v13, v183
	s_nop 1
	v_mfma_scale_f32_16x16x128_f8f6f4 v[178:181], v[8:13], v[44:49], v[178:181], v184, v212 op_sel_hi:[0,0,0] cbsz:2 blgp:2
	v_mov_b32_e32 v6, v186
	v_mov_b32_e32 v7, v187
	s_nop 1
	v_mfma_scale_f32_16x16x128_f8f6f4 v[174:177], v[2:7], v[44:49], v[174:177], v188, v212 op_sel_hi:[0,0,0] cbsz:2 blgp:2
	s_nop 1
	v_mfma_scale_f32_16x16x128_f8f6f4 v[162:165], v[8:13], v[38:43], v[162:165], v184, v208 op_sel_hi:[0,0,0] cbsz:2 blgp:2
	s_nop 1
	v_mfma_scale_f32_16x16x128_f8f6f4 v[158:161], v[2:7], v[38:43], v[158:161], v188, v208 op_sel_hi:[0,0,0] cbsz:2 blgp:2
	s_nop 1
	v_mfma_scale_f32_16x16x128_f8f6f4 v[146:149], v[8:13], v[32:37], v[146:149], v184, v204 op_sel_hi:[0,0,0] cbsz:2 blgp:2
	s_nop 1
	v_mfma_scale_f32_16x16x128_f8f6f4 v[138:141], v[2:7], v[32:37], v[138:141], v188, v204 op_sel_hi:[0,0,0] cbsz:2 blgp:2
	s_nop 1
	v_mfma_scale_f32_16x16x128_f8f6f4 v[126:129], v[8:13], v[26:31], v[126:129], v184, v200 op_sel_hi:[0,0,0] cbsz:2 blgp:2
	s_nop 1
	v_mfma_scale_f32_16x16x128_f8f6f4 v[98:101], v[2:7], v[26:31], v[98:101], v188, v200 op_sel_hi:[0,0,0] cbsz:2 blgp:2
	s_setprio 1
	s_barrier
	ds_read_b128 v[26:29], v224 offset:16384
	ds_read_b128 v[198:201], v224 offset:17408
	ds_read_b128 v[32:35], v224 offset:18432
	ds_read_b128 v[202:205], v224 offset:19456
	ds_read_b128 v[38:41], v224 offset:20480
	ds_read_b128 v[206:209], v224 offset:21504
	ds_read_b128 v[44:47], v224 offset:22528
	ds_read_b128 v[210:213], v224 offset:23552
	s_mov_b32 s17, m0
	s_mov_b32 m0, s47
	s_nop 0
	global_load_lds_dwordx4 v217, s[54:55]
	s_mov_b32 m0, s17
	s_add_u32 s86, s54, 0x40000
	s_mov_b32 s17, m0
	s_mov_b32 m0, s66
	s_nop 0
	global_load_lds_dwordx4 v218, s[54:55]
	s_mov_b32 m0, s17
	s_addc_u32 s87, s55, 0
	s_mov_b32 s17, m0
	s_mov_b32 m0, s67
	s_nop 0
	global_load_lds_dwordx4 v217, s[86:87]
	s_mov_b32 m0, s17
	s_nop 0
	s_mov_b32 s17, m0
	s_mov_b32 m0, s68
	s_nop 0
	global_load_lds_dwordx4 v218, s[86:87]
	s_mov_b32 m0, s17
	s_nop 0
	s_mov_b32 s17, m0
	s_mov_b32 m0, s35
	s_nop 0
	global_load_lds_dwordx4 v50, s[58:59]
	s_mov_b32 m0, s17
	s_nop 0
	s_mov_b32 s17, m0
	s_mov_b32 m0, s69
	s_nop 0
	global_load_lds_dwordx4 v51, s[58:59]
	s_mov_b32 m0, s17
	s_waitcnt vmcnt(8)
	s_waitcnt lgkmcnt(0)
	s_barrier
	s_setprio 0
	s_waitcnt lgkmcnt(6)
	v_mov_b32_e32 v30, v198
	v_mov_b32_e32 v31, v199
	s_nop 1
	v_mfma_scale_f32_16x16x128_f8f6f4 v[114:117], v[20:25], v[26:31], v[114:117], v196, v200 op_sel_hi:[0,0,0] cbsz:2 blgp:2
	s_nop 1
	v_mfma_scale_f32_16x16x128_f8f6f4 v[106:109], v[14:19], v[26:31], v[106:109], v192, v200 op_sel_hi:[0,0,0] cbsz:2 blgp:2
	s_waitcnt lgkmcnt(4)
	v_mov_b32_e32 v36, v202
	v_mov_b32_e32 v37, v203
	s_nop 1
	v_mfma_scale_f32_16x16x128_f8f6f4 v[94:97], v[20:25], v[32:37], v[94:97], v196, v204 op_sel_hi:[0,0,0] cbsz:2 blgp:2
	s_nop 1
	v_mfma_scale_f32_16x16x128_f8f6f4 v[86:89], v[14:19], v[32:37], v[86:89], v192, v204 op_sel_hi:[0,0,0] cbsz:2 blgp:2
	s_waitcnt lgkmcnt(2)
	v_mov_b32_e32 v42, v206
	v_mov_b32_e32 v43, v207
	s_nop 1
	v_mfma_scale_f32_16x16x128_f8f6f4 v[78:81], v[20:25], v[38:43], v[78:81], v196, v208 op_sel_hi:[0,0,0] cbsz:2 blgp:2
	s_nop 1
	v_mfma_scale_f32_16x16x128_f8f6f4 v[70:73], v[14:19], v[38:43], v[70:73], v192, v208 op_sel_hi:[0,0,0] cbsz:2 blgp:2
	s_waitcnt lgkmcnt(0)
	v_mov_b32_e32 v48, v210
	v_mov_b32_e32 v49, v211
	s_nop 1
	v_mfma_scale_f32_16x16x128_f8f6f4 v[62:65], v[20:25], v[44:49], v[62:65], v196, v212 op_sel_hi:[0,0,0] cbsz:2 blgp:2
	s_nop 1
	v_mfma_scale_f32_16x16x128_f8f6f4 v[58:61], v[14:19], v[44:49], v[58:61], v192, v212 op_sel_hi:[0,0,0] cbsz:2 blgp:2
	s_setprio 1
	s_setprio 0
	s_nop 1
	v_mfma_scale_f32_16x16x128_f8f6f4 v[130:133], v[8:13], v[26:31], v[130:133], v184, v200 op_sel_hi:[0,0,0] cbsz:2 blgp:2
	s_nop 1
	v_mfma_scale_f32_16x16x128_f8f6f4 v[122:125], v[2:7], v[26:31], v[122:125], v188, v200 op_sel_hi:[0,0,0] cbsz:2 blgp:2
	s_nop 1
	v_mfma_scale_f32_16x16x128_f8f6f4 v[102:105], v[8:13], v[32:37], v[102:105], v184, v204 op_sel_hi:[0,0,0] cbsz:2 blgp:2
	s_nop 1
	v_mfma_scale_f32_16x16x128_f8f6f4 v[90:93], v[2:7], v[32:37], v[90:93], v188, v204 op_sel_hi:[0,0,0] cbsz:2 blgp:2
	s_nop 1
	v_mfma_scale_f32_16x16x128_f8f6f4 v[82:85], v[8:13], v[38:43], v[82:85], v184, v208 op_sel_hi:[0,0,0] cbsz:2 blgp:2
	s_nop 1
	v_mfma_scale_f32_16x16x128_f8f6f4 v[74:77], v[2:7], v[38:43], v[74:77], v188, v208 op_sel_hi:[0,0,0] cbsz:2 blgp:2
	s_nop 1
	v_mfma_scale_f32_16x16x128_f8f6f4 v[66:69], v[8:13], v[44:49], v[66:69], v184, v212 op_sel_hi:[0,0,0] cbsz:2 blgp:2
	s_nop 1
	v_mfma_scale_f32_16x16x128_f8f6f4 v[54:57], v[2:7], v[44:49], v[54:57], v188, v212 op_sel_hi:[0,0,0] cbsz:2 blgp:2
	s_setprio 1
	s_barrier
; #define PG8_STAGEAS(bufoff, gbase, h) PG8_STAGE2(bufoff, gbase, voffA[h][0], voffA[h][1])
; #define PG8_LDA(dst, b, h) do { _Pragma("unroll") for (int m = 0; m < 4; ++m) _Pragma("unroll") for (int k = 0; k < 2; ++k) dst[m][k] = *(const LAS bf16x8*)(lds + PG8_SA(b, h) + aoff + m * 2048 + k * 1024); } while (0)
; #define PG8_LDB(dst, b, h) do { _Pragma("unroll") for (int n = 0; n < 2; ++n) _Pragma("unroll") for (int k = 0; k < 2; ++k) dst[n][k] = *(const LAS bf16x8*)(lds + PG8_SB(b, h) + boff + n * 2048 + k * 1024); } while (0)
; #define PG8_WAIT_K() do { if constexpr (HM) PG8_WAIT_V(6); else PG8_WAIT_V(8); } while (0)
; #define PG8_WAIT_L(n) asm volatile("s_waitcnt lgkmcnt(" #n ")" ::: "memory")
; #define PG8_BAR __builtin_amdgcn_s_barrier()
; #define PG8_SCHED __builtin_amdgcn_sched_barrier(0)
;     ...
;             PG8_LDB(B0, 1, 0); PG8_LDB(B1, 1, 1); PG8_SCHED; PG8_LDA(At, 1, 0); if constexpr (!HM) PG8_STAGEAS(PG8_SA(0, 1), a2, 1);
;             PG8_WAIT_K(); PG8_WAIT_L(0); PG8_BAR; PG8_MMA(0, 0, At, B0); PG8_MMA(0, 1, At, B1); PG8_BAR; PG8_SCHED;
	ds_read_b128 v[20:23], v232
	ds_read_b128 v[38:41], v232 offset:1024
	ds_read_b128 v[14:17], v232 offset:2048
	ds_read_b128 v[34:37], v232 offset:3072
	ds_read_b128 v[8:11], v233
	ds_read_b128 v[30:33], v233 offset:1024
	ds_read_b128 v[2:5], v233 offset:2048
	ds_read_b128 v[26:29], v233 offset:3072
	ds_read_b128 v[42:45], v224 offset:32768
	ds_read_b128 v[46:49], v224 offset:33792
	ds_read_b128 v[182:185], v224 offset:34816
	ds_read_b128 v[198:201], v224 offset:35840
	ds_read_b128 v[188:191], v224 offset:36864
	ds_read_b128 v[202:205], v224 offset:37888
	ds_read_b128 v[194:197], v224 offset:38912
	ds_read_b128 v[206:209], v224 offset:39936
	s_mov_b32 s17, m0
	s_mov_b32 m0, s70
	s_nop 0
	global_load_lds_dwordx4 v52, s[58:59]
	s_mov_b32 m0, s17
	s_nop 0
	s_mov_b32 s17, m0
	s_mov_b32 m0, s71
	s_nop 0
	global_load_lds_dwordx4 v53, s[58:59]
	s_mov_b32 m0, s17
	s_waitcnt vmcnt(8)
	s_waitcnt lgkmcnt(0)
	s_barrier
	s_setprio 0
	s_waitcnt lgkmcnt(14)
	v_mov_b32_e32 v24, v38
	v_mov_b32_e32 v25, v39
	s_waitcnt lgkmcnt(6)
	s_nop 1
	v_mfma_scale_f32_16x16x128_f8f6f4 v[170:173], v[20:25], v[42:47], v[170:173], v40, v48 op_sel_hi:[0,0,0] cbsz:2 blgp:2
	v_mov_b32_e32 v18, v34
	v_mov_b32_e32 v19, v35
	s_nop 1
	v_mfma_scale_f32_16x16x128_f8f6f4 v[166:169], v[14:19], v[42:47], v[166:169], v36, v48 op_sel_hi:[0,0,0] cbsz:2 blgp:2
	s_waitcnt lgkmcnt(4)
	v_mov_b32_e32 v186, v198
	v_mov_b32_e32 v187, v199
	s_nop 1
	v_mfma_scale_f32_16x16x128_f8f6f4 v[154:157], v[20:25], v[182:187], v[154:157], v40, v200 op_sel_hi:[0,0,0] cbsz:2 blgp:2
	s_nop 1
	v_mfma_scale_f32_16x16x128_f8f6f4 v[150:153], v[14:19], v[182:187], v[150:153], v36, v200 op_sel_hi:[0,0,0] cbsz:2 blgp:2
	s_waitcnt lgkmcnt(2)
	v_mov_b32_e32 v192, v202
	v_mov_b32_e32 v193, v203
	s_nop 1
	v_mfma_scale_f32_16x16x128_f8f6f4 v[142:145], v[20:25], v[188:193], v[142:145], v40, v204 op_sel_hi:[0,0,0] cbsz:2 blgp:2
	s_nop 1
	v_mfma_scale_f32_16x16x128_f8f6f4 v[134:137], v[14:19], v[188:193], v[134:137], v36, v204 op_sel_hi:[0,0,0] cbsz:2 blgp:2
	s_waitcnt lgkmcnt(0)
	v_mov_b32_e32 v198, v206
	v_mov_b32_e32 v199, v207
	s_nop 1
	v_mfma_scale_f32_16x16x128_f8f6f4 v[118:121], v[20:25], v[194:199], v[118:121], v40, v208 op_sel_hi:[0,0,0] cbsz:2 blgp:2
	s_nop 1
	v_mfma_scale_f32_16x16x128_f8f6f4 v[110:113], v[14:19], v[194:199], v[110:113], v36, v208 op_sel_hi:[0,0,0] cbsz:2 blgp:2
	s_setprio 1
	s_setprio 0
	v_mov_b32_e32 v12, v30
	v_mov_b32_e32 v13, v31
	s_nop 1
	v_mfma_scale_f32_16x16x128_f8f6f4 v[178:181], v[8:13], v[42:47], v[178:181], v32, v48 op_sel_hi:[0,0,0] cbsz:2 blgp:2
	v_mov_b32_e32 v6, v26
	v_mov_b32_e32 v7, v27
	s_nop 1
	v_mfma_scale_f32_16x16x128_f8f6f4 v[174:177], v[2:7], v[42:47], v[174:177], v28, v48 op_sel_hi:[0,0,0] cbsz:2 blgp:2
	s_nop 1
	v_mfma_scale_f32_16x16x128_f8f6f4 v[162:165], v[8:13], v[182:187], v[162:165], v32, v200 op_sel_hi:[0,0,0] cbsz:2 blgp:2
	s_nop 1
	v_mfma_scale_f32_16x16x128_f8f6f4 v[158:161], v[2:7], v[182:187], v[158:161], v28, v200 op_sel_hi:[0,0,0] cbsz:2 blgp:2
	s_nop 1
	v_mfma_scale_f32_16x16x128_f8f6f4 v[146:149], v[8:13], v[188:193], v[146:149], v32, v204 op_sel_hi:[0,0,0] cbsz:2 blgp:2
	s_nop 1
	v_mfma_scale_f32_16x16x128_f8f6f4 v[138:141], v[2:7], v[188:193], v[138:141], v28, v204 op_sel_hi:[0,0,0] cbsz:2 blgp:2
	s_nop 1
	v_mfma_scale_f32_16x16x128_f8f6f4 v[126:129], v[8:13], v[194:199], v[126:129], v32, v208 op_sel_hi:[0,0,0] cbsz:2 blgp:2
	s_nop 1
	v_mfma_scale_f32_16x16x128_f8f6f4 v[98:101], v[2:7], v[194:199], v[98:101], v28, v208 op_sel_hi:[0,0,0] cbsz:2 blgp:2
	s_setprio 1
	s_barrier
; #define PG8_STAGEB(bufoff, gbase) PG8_STAGE2(bufoff, gbase, voffB[0], voffB[1])
; #define PG8_STAGEAS(bufoff, gbase, h) PG8_STAGE2(bufoff, gbase, voffA[h][0], voffA[h][1])
; #define PG8_LDA(dst, b, h) do { _Pragma("unroll") for (int m = 0; m < 4; ++m) _Pragma("unroll") for (int k = 0; k < 2; ++k) dst[m][k] = *(const LAS bf16x8*)(lds + PG8_SA(b, h) + aoff + m * 2048 + k * 1024); } while (0)
; #define PG8_WAIT_K() do { if constexpr (HM) PG8_WAIT_V(6); else PG8_WAIT_V(8); } while (0)
; #define PG8_WAIT_L(n) asm volatile("s_waitcnt lgkmcnt(" #n ")" ::: "memory")
; #define PG8_BAR __builtin_amdgcn_s_barrier()
; #define PG8_SCHED __builtin_amdgcn_sched_barrier(0)
;     ...
;             if constexpr (!HM) PG8_LDA(At, 1, 1);
;             PG8_STAGEB(PG8_SB(1, 0), b3); PG8_STAGEB(PG8_SB(1, 1), b3 + hstepB); PG8_STAGEAS(PG8_SA(1, 0), a3, 0);
;             PG8_WAIT_K(); PG8_WAIT_L(0); PG8_BAR; if constexpr (!HM) { PG8_MMA(1, 0, At, B0); PG8_MMA(1, 1, At, B1); } PG8_BAR; PG8_SCHED;
	ds_read_b128 v[42:45], v224 offset:49152
	ds_read_b128 v[46:49], v224 offset:50176
	ds_read_b128 v[182:185], v224 offset:51200
	ds_read_b128 v[198:201], v224 offset:52224
	ds_read_b128 v[188:191], v224 offset:53248
	ds_read_b128 v[202:205], v224 offset:54272
	ds_read_b128 v[194:197], v224 offset:55296
	ds_read_b128 v[206:209], v224 offset:56320
	s_mov_b32 s17, m0
	s_mov_b32 m0, s72
	s_nop 0
	global_load_lds_dwordx4 v217, s[56:57]
	s_mov_b32 m0, s17
	s_add_u32 s54, s54, 0x40080
	s_mov_b32 s17, m0
	s_mov_b32 m0, s73
	s_nop 0
	global_load_lds_dwordx4 v218, s[56:57]
	s_mov_b32 m0, s17
	s_addc_u32 s55, s55, 0
	s_mov_b32 s17, m0
	s_mov_b32 m0, s76
	s_nop 0
	global_load_lds_dwordx4 v217, s[54:55]
	s_mov_b32 m0, s17
	s_nop 0
	s_mov_b32 s17, m0
	s_mov_b32 m0, s77
	s_nop 0
	global_load_lds_dwordx4 v218, s[54:55]
	s_mov_b32 m0, s17
	s_nop 0
	s_mov_b32 s17, m0
	s_mov_b32 m0, s74
	s_nop 0
	global_load_lds_dwordx4 v50, s[52:53]
	s_mov_b32 m0, s17
	s_nop 0
	s_mov_b32 s17, m0
	s_mov_b32 m0, s75
	s_nop 0
	global_load_lds_dwordx4 v51, s[52:53]
	s_mov_b32 m0, s17
	s_waitcnt vmcnt(8)
	s_waitcnt lgkmcnt(0)
	s_barrier
	s_setprio 0
	s_waitcnt lgkmcnt(6)
	s_nop 1
	v_mfma_scale_f32_16x16x128_f8f6f4 v[114:117], v[20:25], v[42:47], v[114:117], v40, v48 op_sel_hi:[0,0,0] cbsz:2 blgp:2
	s_nop 1
	v_mfma_scale_f32_16x16x128_f8f6f4 v[106:109], v[14:19], v[42:47], v[106:109], v36, v48 op_sel_hi:[0,0,0] cbsz:2 blgp:2
	s_waitcnt lgkmcnt(4)
	v_mov_b32_e32 v186, v198
	v_mov_b32_e32 v187, v199
	s_nop 1
	v_mfma_scale_f32_16x16x128_f8f6f4 v[94:97], v[20:25], v[182:187], v[94:97], v40, v200 op_sel_hi:[0,0,0] cbsz:2 blgp:2
	s_nop 1
	v_mfma_scale_f32_16x16x128_f8f6f4 v[86:89], v[14:19], v[182:187], v[86:89], v36, v200 op_sel_hi:[0,0,0] cbsz:2 blgp:2
	s_waitcnt lgkmcnt(2)
	v_mov_b32_e32 v192, v202
	v_mov_b32_e32 v193, v203
	s_nop 1
	v_mfma_scale_f32_16x16x128_f8f6f4 v[78:81], v[20:25], v[188:193], v[78:81], v40, v204 op_sel_hi:[0,0,0] cbsz:2 blgp:2
	s_nop 1
	v_mfma_scale_f32_16x16x128_f8f6f4 v[70:73], v[14:19], v[188:193], v[70:73], v36, v204 op_sel_hi:[0,0,0] cbsz:2 blgp:2
	s_waitcnt lgkmcnt(0)
	v_mov_b32_e32 v198, v206
	v_mov_b32_e32 v199, v207
	s_nop 1
	v_mfma_scale_f32_16x16x128_f8f6f4 v[62:65], v[20:25], v[194:199], v[62:65], v40, v208 op_sel_hi:[0,0,0] cbsz:2 blgp:2
	s_nop 1
	v_mfma_scale_f32_16x16x128_f8f6f4 v[58:61], v[14:19], v[194:199], v[58:61], v36, v208 op_sel_hi:[0,0,0] cbsz:2 blgp:2
	s_setprio 1
	s_setprio 0
	s_nop 1
	v_mfma_scale_f32_16x16x128_f8f6f4 v[130:133], v[8:13], v[42:47], v[130:133], v32, v48 op_sel_hi:[0,0,0] cbsz:2 blgp:2
	s_nop 1
	v_mfma_scale_f32_16x16x128_f8f6f4 v[122:125], v[2:7], v[42:47], v[122:125], v28, v48 op_sel_hi:[0,0,0] cbsz:2 blgp:2
	s_nop 1
	v_mfma_scale_f32_16x16x128_f8f6f4 v[102:105], v[8:13], v[182:187], v[102:105], v32, v200 op_sel_hi:[0,0,0] cbsz:2 blgp:2
	s_nop 1
	v_mfma_scale_f32_16x16x128_f8f6f4 v[90:93], v[2:7], v[182:187], v[90:93], v28, v200 op_sel_hi:[0,0,0] cbsz:2 blgp:2
	s_nop 1
	v_mfma_scale_f32_16x16x128_f8f6f4 v[82:85], v[8:13], v[188:193], v[82:85], v32, v204 op_sel_hi:[0,0,0] cbsz:2 blgp:2
	s_nop 1
	v_mfma_scale_f32_16x16x128_f8f6f4 v[74:77], v[2:7], v[188:193], v[74:77], v28, v204 op_sel_hi:[0,0,0] cbsz:2 blgp:2
	s_nop 1
	v_mfma_scale_f32_16x16x128_f8f6f4 v[66:69], v[8:13], v[194:199], v[66:69], v32, v208 op_sel_hi:[0,0,0] cbsz:2 blgp:2
	s_nop 1
	v_mfma_scale_f32_16x16x128_f8f6f4 v[54:57], v[2:7], v[194:199], v[54:57], v28, v208 op_sel_hi:[0,0,0] cbsz:2 blgp:2
	s_setprio 1
	s_barrier
	s_add_i32 s16, s16, 2
	s_add_u32 s18, s18, 0x100
	s_addc_u32 s19, s19, 0
	s_cmp_gt_u32 s16, 13
	s_cbranch_scc1 .LBB0_1140

; #define LAS __attribute__((address_space(3)))
; #define PG8_STAGEB(bufoff, gbase) PG8_STAGE2(bufoff, gbase, voffB[0], voffB[1])
; #define PG8_STAGEA(bufoff, gbase, h) PG8_STAGE2(bufoff, gbase, voffA[h][0], voffA[h][1])
; #define PG8_STAGEAS(bufoff, gbase, h) PG8_STAGE2(bufoff, gbase, voffA[h][0], voffA[h][1])
; #define PG8_LDA(dst, b, h) do { _Pragma("unroll") for (int m = 0; m < 4; ++m) _Pragma("unroll") for (int k = 0; k < 2; ++k) dst[m][k] = *(const LAS bf16x8*)(lds + PG8_SA(b, h) + aoff + m * 2048 + k * 1024); } while (0)
; #define PG8_LDB(dst, b, h) do { _Pragma("unroll") for (int n = 0; n < 2; ++n) _Pragma("unroll") for (int k = 0; k < 2; ++k) dst[n][k] = *(const LAS bf16x8*)(lds + PG8_SB(b, h) + boff + n * 2048 + k * 1024); } while (0)
; #define PG8_WAIT_K0() do { if (EST > 0 && t == 0 && ui > 0) asm volatile("s_waitcnt vmcnt(%0)" :: "n"((HM ? 6 : 8) + EST) : "memory"); else PG8_WAIT_K(); } while (0)
; #define PG8_WAIT_L(n) asm volatile("s_waitcnt lgkmcnt(" #n ")" ::: "memory")
; #define PG8_BAR __builtin_amdgcn_s_barrier()
; #define PG8_SCHED __builtin_amdgcn_sched_barrier(0)
;     ...
;             PG8_LDB(B0, 0, 0); PG8_LDB(B1, 0, 1); PG8_SCHED; PG8_LDA(At, 0, 0); if constexpr (!HM) PG8_STAGEA(PG8_SA(1, 1), a1, 1);
;             if constexpr (Sched::kGather) { if (last && has_next) { const u32x4 tn = *(const LAS u32x4*)(S.aux + tid * 16); voffA[0][0] = tn.x; voffA[0][1] = tn.y; voffA[1][0] = tn.z; voffA[1][1] = tn.w; } }
;             PG8_WAIT_K0(); PG8_WAIT_L(0); PG8_BAR; PG8_MMA(0, 0, At, B0); PG8_MMA(0, 1, At, B1); PG8_BAR; PG8_SCHED;
;             if constexpr (!HM) PG8_LDA(At, 0, 1);
;             PG8_STAGEB(PG8_SB(0, 0), b2); PG8_STAGEB(PG8_SB(0, 1), b2 + hstepB); PG8_STAGEAS(PG8_SA(0, 0), a2, 0);
;             PG8_WAIT_K0(); PG8_WAIT_L(0); PG8_BAR; if constexpr (!HM) { PG8_MMA(1, 0, At, B0); PG8_MMA(1, 1, At, B1); } PG8_BAR; PG8_SCHED;
.LBB0_1181:
	s_waitcnt lgkmcnt(0)
	s_add_u32 s50, s46, 0x100
	s_addc_u32 s51, s47, 0
	s_barrier
	s_setprio 0
	s_waitcnt lgkmcnt(6)
	v_mov_b32_e32 v36, v80
	v_mov_b32_e32 v37, v81
	v_mov_b64_e32 v[108:109], s[14:15]
	v_mov_b32_e32 v42, v92
	v_mov_b32_e32 v43, v93
	v_mov_b64_e32 v[104:105], s[14:15]
	s_waitcnt lgkmcnt(4)
	v_mov_b32_e32 v30, v72
	v_mov_b32_e32 v31, v73
	v_mov_b64_e32 v[92:93], s[14:15]
	v_mov_b64_e32 v[88:89], s[14:15]
	s_waitcnt lgkmcnt(2)
	v_mov_b32_e32 v24, v64
	v_mov_b32_e32 v25, v65
	v_mov_b64_e32 v[80:81], s[14:15]
	v_mov_b64_e32 v[72:73], s[14:15]
	v_mov_b64_e32 v[64:65], s[14:15]
	v_mov_b64_e32 v[106:107], s[12:13]
	v_mov_b64_e32 v[102:103], s[12:13]
	v_mov_b64_e32 v[90:91], s[12:13]
	v_mov_b64_e32 v[86:87], s[12:13]
	v_mov_b64_e32 v[78:79], s[12:13]
	v_mov_b64_e32 v[70:71], s[12:13]
	v_mov_b64_e32 v[62:63], s[12:13]
	v_mov_b32_e32 v48, v56
	v_mov_b32_e32 v49, v57
	v_mov_b64_e32 v[56:57], s[14:15]
	s_nop 1
	v_mfma_scale_f32_16x16x128_f8f6f4 v[106:109], v[44:49], v[32:37], v[106:109], v58, v82 op_sel_hi:[0,0,0] cbsz:2 blgp:2
	s_nop 1
	v_mfma_scale_f32_16x16x128_f8f6f4 v[102:105], v[38:43], v[32:37], v[102:105], v94, v82 op_sel_hi:[0,0,0] cbsz:2 blgp:2
	s_nop 1
	v_mfma_scale_f32_16x16x128_f8f6f4 v[90:93], v[44:49], v[26:31], v[90:93], v58, v74 op_sel_hi:[0,0,0] cbsz:2 blgp:2
	s_nop 1
	v_mfma_scale_f32_16x16x128_f8f6f4 v[86:89], v[38:43], v[26:31], v[86:89], v94, v74 op_sel_hi:[0,0,0] cbsz:2 blgp:2
	s_nop 1
	v_mfma_scale_f32_16x16x128_f8f6f4 v[78:81], v[44:49], v[20:25], v[78:81], v58, v66 op_sel_hi:[0,0,0] cbsz:2 blgp:2
	s_nop 1
	v_mfma_scale_f32_16x16x128_f8f6f4 v[70:73], v[38:43], v[20:25], v[70:73], v94, v66 op_sel_hi:[0,0,0] cbsz:2 blgp:2
	s_waitcnt lgkmcnt(0)
	v_mov_b32_e32 v18, v126
	v_mov_b32_e32 v19, v127
	s_nop 1
	v_mfma_scale_f32_16x16x128_f8f6f4 v[62:65], v[44:49], v[14:19], v[62:65], v58, v128 op_sel_hi:[0,0,0] cbsz:2 blgp:2
	v_mov_b64_e32 v[60:61], s[14:15]
	v_mov_b64_e32 v[54:55], s[12:13]
	v_mov_b64_e32 v[58:59], s[12:13]
	s_nop 1
	v_mfma_scale_f32_16x16x128_f8f6f4 v[58:61], v[38:43], v[14:19], v[58:61], v94, v128 op_sel_hi:[0,0,0] cbsz:2 blgp:2
	s_setprio 1
	s_setprio 0
	v_mov_b64_e32 v[116:117], s[14:15]
	v_mov_b64_e32 v[112:113], s[14:15]
	v_mov_b64_e32 v[100:101], s[14:15]
	v_mov_b64_e32 v[96:97], s[14:15]
	v_mov_b64_e32 v[114:115], s[12:13]
	v_mov_b64_e32 v[110:111], s[12:13]
	v_mov_b64_e32 v[98:99], s[12:13]
	v_mov_b64_e32 v[94:95], s[12:13]
	v_mov_b32_e32 v12, v122
	v_mov_b32_e32 v13, v123
	s_nop 1
	v_mfma_scale_f32_16x16x128_f8f6f4 v[114:117], v[8:13], v[32:37], v[114:117], v124, v82 op_sel_hi:[0,0,0] cbsz:2 blgp:2
	v_mov_b32_e32 v6, v118
	v_mov_b32_e32 v7, v119
	s_nop 1
	v_mfma_scale_f32_16x16x128_f8f6f4 v[110:113], v[2:7], v[32:37], v[110:113], v120, v82 op_sel_hi:[0,0,0] cbsz:2 blgp:2
	s_nop 1
	v_mfma_scale_f32_16x16x128_f8f6f4 v[98:101], v[8:13], v[26:31], v[98:101], v124, v74 op_sel_hi:[0,0,0] cbsz:2 blgp:2
	s_nop 1
	v_mfma_scale_f32_16x16x128_f8f6f4 v[94:97], v[2:7], v[26:31], v[94:97], v120, v74 op_sel_hi:[0,0,0] cbsz:2 blgp:2
	v_mov_b64_e32 v[84:85], s[14:15]
	v_mov_b64_e32 v[76:77], s[14:15]
	v_mov_b64_e32 v[82:83], s[12:13]
	v_mov_b64_e32 v[74:75], s[12:13]
	s_nop 1
	v_mfma_scale_f32_16x16x128_f8f6f4 v[82:85], v[8:13], v[20:25], v[82:85], v124, v66 op_sel_hi:[0,0,0] cbsz:2 blgp:2
	s_nop 1
	v_mfma_scale_f32_16x16x128_f8f6f4 v[74:77], v[2:7], v[20:25], v[74:77], v120, v66 op_sel_hi:[0,0,0] cbsz:2 blgp:2
	v_mov_b64_e32 v[68:69], s[14:15]
	v_mov_b64_e32 v[66:67], s[12:13]
	s_nop 1
	v_mfma_scale_f32_16x16x128_f8f6f4 v[66:69], v[8:13], v[14:19], v[66:69], v124, v128 op_sel_hi:[0,0,0] cbsz:2 blgp:2
	s_nop 1
	v_mfma_scale_f32_16x16x128_f8f6f4 v[54:57], v[2:7], v[14:19], v[54:57], v120, v128 op_sel_hi:[0,0,0] cbsz:2 blgp:2
	s_setprio 1
	s_barrier
	s_mov_b32 s39, m0
	s_mov_b32 m0, s45
	s_nop 0
	global_load_lds_dwordx4 v153, s[50:51]
	s_mov_b32 m0, s39
	s_nop 0
	s_mov_b32 s39, m0
	s_mov_b32 m0, s62
	s_nop 0
	global_load_lds_dwordx4 v154, s[50:51]
	s_mov_b32 m0, s39
	s_add_u32 s50, s46, 0x40100
	s_addc_u32 s51, s47, 0
	s_mov_b32 s39, m0
	s_mov_b32 m0, s63
	s_nop 0
	global_load_lds_dwordx4 v153, s[50:51]
	s_mov_b32 m0, s39
	s_and_b64 vcc, exec, s[48:49]
	s_mov_b32 s39, m0
	s_mov_b32 m0, s64
	s_nop 0
	global_load_lds_dwordx4 v154, s[50:51]
	s_mov_b32 m0, s39
	s_nop 0
	s_mov_b32 s39, m0
	s_mov_b32 m0, s17
	s_nop 0
	global_load_lds_dwordx4 v50, s[24:25]
	s_mov_b32 m0, s39
	s_nop 0
	s_mov_b32 s39, m0
	s_mov_b32 m0, s65
	s_nop 0
	global_load_lds_dwordx4 v51, s[24:25]
	s_mov_b32 m0, s39
	s_cbranch_vccz .LBB0_1198
	s_waitcnt vmcnt(10)
	s_cbranch_execnz .LBB0_1184

; #define LAS __attribute__((address_space(3)))
; #define PG8_RC() int R[2], C[2]; { int t_ = threadIdx.x; asm volatile("" : "+v"(t_)); _Pragma("unroll") for (int i = 0; i < 2; ++i) stage_rc(t_ * 16 + i * 8192, R[i], C[i]); }
; #define PG8_STAGEB(bufoff, gbase) PG8_STAGE2(bufoff, gbase, voffB[0], voffB[1])
; #define PG8_STAGEAS(bufoff, gbase, h) PG8_STAGE2(bufoff, gbase, voffA[h][0], voffA[h][1])
; #define PG8_LDA(dst, b, h) do { _Pragma("unroll") for (int m = 0; m < 4; ++m) _Pragma("unroll") for (int k = 0; k < 2; ++k) dst[m][k] = *(const LAS bf16x8*)(lds + PG8_SA(b, h) + aoff + m * 2048 + k * 1024); } while (0)
; #define PG8_LDB(dst, b, h) do { _Pragma("unroll") for (int n = 0; n < 2; ++n) _Pragma("unroll") for (int k = 0; k < 2; ++k) dst[n][k] = *(const LAS bf16x8*)(lds + PG8_SB(b, h) + boff + n * 2048 + k * 1024); } while (0)
; #define PG8_WAIT_K() do { if constexpr (HM) PG8_WAIT_V(6); else PG8_WAIT_V(8); } while (0)
; #define PG8_WAIT_L(n) asm volatile("s_waitcnt lgkmcnt(" #n ")" ::: "memory")
; #define PG8_BAR __builtin_amdgcn_s_barrier()
;     ...
;                 if (t == 2 && has_next) {
;                     if constexpr (HM) asm volatile("s_waitcnt vmcnt(12)" : "+v"(gtok0), "+v"(gtok1), "+v"(gtok2), "+v"(gtok3) :: "memory");
;                     else asm volatile("s_waitcnt vmcnt(16)" : "+v"(gtok0), "+v"(gtok1), "+v"(gtok2), "+v"(gtok3) :: "memory");
;                     PG8_RC(); *(LAS u32x4*)(S.aux + tid * 16) = (u32x4){(unsigned)(((int)gtok0 >> 2) * S.lda + C[0]) * 2u, (unsigned)(((int)gtok1 >> 2) * S.lda + C[1]) * 2u, (unsigned)(((int)gtok2 >> 2) * S.lda + C[0]) * 2u, (unsigned)(((int)gtok3 >> 2) * S.lda + C[1]) * 2u};
;     ...
;             PG8_WAIT_K0(); PG8_WAIT_L(0); PG8_BAR; if constexpr (!HM) { PG8_MMA(1, 0, At, B0); PG8_MMA(1, 1, At, B1); } PG8_BAR; PG8_SCHED;
;             PG8_LDB(B0, 1, 0); PG8_LDB(B1, 1, 1); PG8_SCHED; PG8_LDA(At, 1, 0); if constexpr (!HM) PG8_STAGEAS(PG8_SA(0, 1), a2, 1);
;             PG8_WAIT_K(); PG8_WAIT_L(0); PG8_BAR; PG8_MMA(0, 0, At, B0); PG8_MMA(0, 1, At, B1); PG8_BAR; PG8_SCHED;
;             if constexpr (!HM) PG8_LDA(At, 1, 1);
;             PG8_STAGEB(PG8_SB(1, 0), b3); PG8_STAGEB(PG8_SB(1, 1), b3 + hstepB); PG8_STAGEAS(PG8_SA(1, 0), a3, 0);
;             PG8_WAIT_K(); PG8_WAIT_L(0); PG8_BAR; if constexpr (!HM) { PG8_MMA(1, 0, At, B0); PG8_MMA(1, 1, At, B1); } PG8_BAR; PG8_SCHED;
.LBB0_1184:
	s_waitcnt lgkmcnt(0)
	s_add_u32 s48, s46, 0x180
	s_addc_u32 s49, s47, 0
	s_barrier
	s_barrier
	v_add_u32_e32 v164, 0x18000, v159
	v_add_u32_e32 v165, 0x1c000, v159
	ds_read_b128 v[2:5], v164
	ds_read_b128 v[118:121], v164 offset:1024
	ds_read_b128 v[8:11], v164 offset:2048
	ds_read_b128 v[122:125], v164 offset:3072
	ds_read_b128 v[14:17], v165
	ds_read_b128 v[126:129], v165 offset:1024
	ds_read_b128 v[20:23], v165 offset:2048
	ds_read_b128 v[132:135], v165 offset:3072
	ds_read_b128 v[26:29], v160 offset:32768
	ds_read_b128 v[136:139], v160 offset:33792
	ds_read_b128 v[32:35], v160 offset:34816
	ds_read_b128 v[140:143], v160 offset:35840
	ds_read_b128 v[38:41], v160 offset:36864
	ds_read_b128 v[144:147], v160 offset:37888
	ds_read_b128 v[44:47], v160 offset:38912
	ds_read_b128 v[166:169], v160 offset:39936
	s_waitcnt vmcnt(6)
	s_waitcnt lgkmcnt(0)
	s_barrier
	s_setprio 0
	s_waitcnt lgkmcnt(6)
	v_mov_b32_e32 v30, v136
	v_mov_b32_e32 v31, v137
	v_mov_b32_e32 v6, v118
	v_mov_b32_e32 v7, v119
	s_nop 1
	v_mfma_scale_f32_16x16x128_f8f6f4 v[106:109], v[2:7], v[26:31], v[106:109], v120, v138 op_sel_hi:[0,0,0] cbsz:2 blgp:2
	v_mov_b32_e32 v12, v122
	v_mov_b32_e32 v13, v123
	s_nop 1
	v_mfma_scale_f32_16x16x128_f8f6f4 v[102:105], v[8:13], v[26:31], v[102:105], v124, v138 op_sel_hi:[0,0,0] cbsz:2 blgp:2
	s_waitcnt lgkmcnt(4)
	v_mov_b32_e32 v36, v140
	v_mov_b32_e32 v37, v141
	s_nop 1
	v_mfma_scale_f32_16x16x128_f8f6f4 v[90:93], v[2:7], v[32:37], v[90:93], v120, v142 op_sel_hi:[0,0,0] cbsz:2 blgp:2
	s_nop 1
	v_mfma_scale_f32_16x16x128_f8f6f4 v[86:89], v[8:13], v[32:37], v[86:89], v124, v142 op_sel_hi:[0,0,0] cbsz:2 blgp:2
	s_waitcnt lgkmcnt(2)
	v_mov_b32_e32 v42, v144
	v_mov_b32_e32 v43, v145
	s_nop 1
	v_mfma_scale_f32_16x16x128_f8f6f4 v[78:81], v[2:7], v[38:43], v[78:81], v120, v146 op_sel_hi:[0,0,0] cbsz:2 blgp:2
	s_nop 1
	v_mfma_scale_f32_16x16x128_f8f6f4 v[70:73], v[8:13], v[38:43], v[70:73], v124, v146 op_sel_hi:[0,0,0] cbsz:2 blgp:2
	s_waitcnt lgkmcnt(0)
	v_mov_b32_e32 v48, v166
	v_mov_b32_e32 v49, v167
	s_nop 1
	v_mfma_scale_f32_16x16x128_f8f6f4 v[62:65], v[2:7], v[44:49], v[62:65], v120, v168 op_sel_hi:[0,0,0] cbsz:2 blgp:2
	s_nop 1
	v_mfma_scale_f32_16x16x128_f8f6f4 v[58:61], v[8:13], v[44:49], v[58:61], v124, v168 op_sel_hi:[0,0,0] cbsz:2 blgp:2
	s_setprio 1
	s_setprio 0
	v_mov_b32_e32 v18, v126
	v_mov_b32_e32 v19, v127
	s_nop 1
	v_mfma_scale_f32_16x16x128_f8f6f4 v[114:117], v[14:19], v[26:31], v[114:117], v128, v138 op_sel_hi:[0,0,0] cbsz:2 blgp:2
	v_mov_b32_e32 v24, v132
	v_mov_b32_e32 v25, v133
	s_nop 1
	v_mfma_scale_f32_16x16x128_f8f6f4 v[110:113], v[20:25], v[26:31], v[110:113], v134, v138 op_sel_hi:[0,0,0] cbsz:2 blgp:2
	s_nop 1
	v_mfma_scale_f32_16x16x128_f8f6f4 v[98:101], v[14:19], v[32:37], v[98:101], v128, v142 op_sel_hi:[0,0,0] cbsz:2 blgp:2
	s_nop 1
	v_mfma_scale_f32_16x16x128_f8f6f4 v[94:97], v[20:25], v[32:37], v[94:97], v134, v142 op_sel_hi:[0,0,0] cbsz:2 blgp:2
	s_nop 1
	v_mfma_scale_f32_16x16x128_f8f6f4 v[82:85], v[14:19], v[38:43], v[82:85], v128, v146 op_sel_hi:[0,0,0] cbsz:2 blgp:2
	s_nop 1
	v_mfma_scale_f32_16x16x128_f8f6f4 v[74:77], v[20:25], v[38:43], v[74:77], v134, v146 op_sel_hi:[0,0,0] cbsz:2 blgp:2
	s_nop 1
	v_mfma_scale_f32_16x16x128_f8f6f4 v[66:69], v[14:19], v[44:49], v[66:69], v128, v168 op_sel_hi:[0,0,0] cbsz:2 blgp:2
	s_nop 1
	v_mfma_scale_f32_16x16x128_f8f6f4 v[54:57], v[20:25], v[44:49], v[54:57], v134, v168 op_sel_hi:[0,0,0] cbsz:2 blgp:2
	s_setprio 1
	s_barrier
	s_mov_b32 s39, m0
	s_mov_b32 m0, s66
	s_nop 0
	global_load_lds_dwordx4 v153, s[48:49]
	s_mov_b32 m0, s39
	s_nop 0
	s_mov_b32 s39, m0
	s_mov_b32 m0, s67
	s_nop 0
	global_load_lds_dwordx4 v154, s[48:49]
	s_mov_b32 m0, s39
	s_add_u32 s48, s46, 0x40180
	s_addc_u32 s49, s47, 0
	s_mov_b32 s39, m0
	s_mov_b32 m0, s70
	s_nop 0
	global_load_lds_dwordx4 v153, s[48:49]
	s_mov_b32 m0, s39
	s_nop 0
	s_mov_b32 s39, m0
	s_mov_b32 m0, s71
	s_nop 0
	global_load_lds_dwordx4 v154, s[48:49]
	s_mov_b32 m0, s39
	s_nop 0
	s_mov_b32 s39, m0
	s_mov_b32 m0, s68
	s_nop 0
	global_load_lds_dwordx4 v50, s[26:27]
	s_mov_b32 m0, s39
	s_nop 0
	s_mov_b32 s39, m0
	s_mov_b32 m0, s69
	s_nop 0
	global_load_lds_dwordx4 v51, s[26:27]
	s_mov_b32 m0, s39
	s_waitcnt vmcnt(6)
	s_waitcnt lgkmcnt(0)
	s_barrier
	s_barrier
	v_add_u32_e32 v2, 0, v152
	s_and_b64 vcc, exec, s[8:9]
	v_add_u32_e32 v166, 0x20000, v2
	s_cbranch_vccnz .LBB0_1186
	v_mov_b32_e32 v2, v0
	s_waitcnt vmcnt(12)
	s_nop 0
	v_ashrrev_i32_e32 v4, 31, v2
	v_lshrrev_b32_e32 v4, 26, v4
	v_lshlrev_b32_e32 v3, 4, v2
	v_add_u32_e32 v4, v2, v4
	v_bfe_i32 v2, v2, 27, 1
	v_lshrrev_b32_e32 v2, 22, v2
	v_add_u32_e32 v2, v3, v2
	v_and_b32_e32 v2, 0xfffffc00, v2
	v_sub_u32_e32 v2, v3, v2
	v_lshrrev_b32_e32 v5, 4, v2
	v_bitop3_b32 v5, v5, v2, 32 bitop3:0x6c
	v_ashrrev_i32_e32 v2, 31, v2
	v_lshrrev_b32_e32 v2, 26, v2
	v_add_u32_e32 v2, v5, v2
	v_and_b32_e32 v2, 0xc0, v2
	v_lshrrev_b32_e32 v4, 1, v4
	v_sub_u32_e32 v2, v5, v2
	v_and_b32_e32 v4, 32, v4
	v_ashrrev_i16_sdwa v2, v1, sext(v2) dst_sel:DWORD dst_unused:UNUSED_PAD src0_sel:DWORD src1_sel:BYTE_0
	v_add_u32_sdwa v4, v4, sext(v2) dst_sel:DWORD dst_unused:UNUSED_PAD src0_sel:DWORD src1_sel:WORD_0
	v_add_u32_e32 v2, 0x2000, v3
	v_ashrrev_i32_e32 v3, 31, v2
	v_lshrrev_b32_e32 v3, 22, v3
	v_add_u32_e32 v3, v2, v3
	v_ashrrev_i32_e32 v3, 10, v3
	v_mul_i32_i24_e32 v5, 0x400, v3
	v_sub_u32_e32 v2, v2, v5
	v_lshrrev_b32_e32 v5, 4, v2
	v_bitop3_b32 v5, v5, v2, 32 bitop3:0x6c
	v_ashrrev_i32_e32 v2, 31, v2
	v_lshrrev_b32_e32 v2, 26, v2
	v_add_u32_e32 v2, v5, v2
	v_and_b32_e32 v2, 0xc0, v2
	v_lshlrev_b32_e32 v3, 5, v3
	v_sub_u32_e32 v2, v5, v2
	v_and_b32_e32 v3, 32, v3
	v_ashrrev_i16_sdwa v2, v1, sext(v2) dst_sel:DWORD dst_unused:UNUSED_PAD src0_sel:DWORD src1_sel:BYTE_0
	v_add_u32_sdwa v5, v3, sext(v2) dst_sel:DWORD dst_unused:UNUSED_PAD src0_sel:DWORD src1_sel:WORD_0
	v_lshlrev_b32_e32 v2, 8, v131
	v_lshlrev_b32_e32 v6, 8, v53
	v_and_b32_e32 v2, 0x7ffffc00, v2
	v_and_b32_e32 v6, 0x7ffffc00, v6
	v_add_lshl_u32 v2, v4, v2, 1
	v_lshlrev_b32_e32 v3, 8, v130
	v_add_lshl_u32 v4, v4, v6, 1
	v_lshlrev_b32_e32 v6, 8, v52
	v_and_b32_e32 v3, 0x7ffffc00, v3
	v_and_b32_e32 v6, 0x7ffffc00, v6
	v_add_lshl_u32 v3, v5, v3, 1
	v_add_lshl_u32 v5, v5, v6, 1
	ds_write_b128 v166, v[2:5]
; #define PG8_STAGEB(bufoff, gbase) PG8_STAGE2(bufoff, gbase, voffB[0], voffB[1])
; #define PG8_STAGEAS(bufoff, gbase, h) PG8_STAGE2(bufoff, gbase, voffA[h][0], voffA[h][1])
; #define PG8_LDA(dst, b, h) do { _Pragma("unroll") for (int m = 0; m < 4; ++m) _Pragma("unroll") for (int k = 0; k < 2; ++k) dst[m][k] = *(const LAS bf16x8*)(lds + PG8_SA(b, h) + aoff + m * 2048 + k * 1024); } while (0)
; #define PG8_LDB(dst, b, h) do { _Pragma("unroll") for (int n = 0; n < 2; ++n) _Pragma("unroll") for (int k = 0; k < 2; ++k) dst[n][k] = *(const LAS bf16x8*)(lds + PG8_SB(b, h) + boff + n * 2048 + k * 1024); } while (0)
; #define PG8_WAIT_K() do { if constexpr (HM) PG8_WAIT_V(6); else PG8_WAIT_V(8); } while (0)
; #define PG8_WAIT_L(n) asm volatile("s_waitcnt lgkmcnt(" #n ")" ::: "memory")
; #define PG8_BAR __builtin_amdgcn_s_barrier()
; #define PG8_SCHED __builtin_amdgcn_sched_barrier(0)
;     ...
;             PG8_LDB(B0, 1, 0); PG8_LDB(B1, 1, 1); PG8_SCHED; PG8_LDA(At, 1, 0); if constexpr (!HM) PG8_STAGEAS(PG8_SA(0, 1), a2, 1);
;             PG8_WAIT_K(); PG8_WAIT_L(0); PG8_BAR; PG8_MMA(0, 0, At, B0); PG8_MMA(0, 1, At, B1); PG8_BAR; PG8_SCHED;
;             if constexpr (!HM) PG8_LDA(At, 1, 1);
;             PG8_STAGEB(PG8_SB(1, 0), b3); PG8_STAGEB(PG8_SB(1, 1), b3 + hstepB); PG8_STAGEAS(PG8_SA(1, 0), a3, 0);
;             PG8_WAIT_K(); PG8_WAIT_L(0); PG8_BAR; if constexpr (!HM) { PG8_MMA(1, 0, At, B0); PG8_MMA(1, 1, At, B1); } PG8_BAR; PG8_SCHED;
.LBB0_1186:
	ds_read_b128 v[2:5], v163
	ds_read_b128 v[118:121], v163 offset:1024
	ds_read_b128 v[8:11], v163 offset:2048
	ds_read_b128 v[122:125], v163 offset:3072
	ds_read_b128 v[14:17], v162
	ds_read_b128 v[126:129], v162 offset:1024
	ds_read_b128 v[20:23], v162 offset:2048
	ds_read_b128 v[130:133], v162 offset:3072
	s_add_u32 s50, s46, 0x200
	s_addc_u32 s51, s47, 0
	ds_read_b128 v[26:29], v160
	ds_read_b128 v[134:137], v160 offset:1024
	ds_read_b128 v[32:35], v160 offset:2048
	ds_read_b128 v[138:141], v160 offset:3072
	ds_read_b128 v[38:41], v160 offset:4096
	ds_read_b128 v[142:145], v160 offset:5120
	ds_read_b128 v[44:47], v160 offset:6144
	ds_read_b128 v[146:149], v160 offset:7168
	s_waitcnt vmcnt(6)
	s_waitcnt lgkmcnt(0)
	s_add_u32 s48, s46, 0x280
	s_addc_u32 s49, s47, 0
	s_barrier
	s_setprio 0
	s_waitcnt lgkmcnt(6)
	v_mov_b32_e32 v30, v134
	v_mov_b32_e32 v31, v135
	v_mov_b32_e32 v6, v118
	v_mov_b32_e32 v7, v119
	s_nop 1
	v_mfma_scale_f32_16x16x128_f8f6f4 v[106:109], v[2:7], v[26:31], v[106:109], v120, v136 op_sel_hi:[0,0,0] cbsz:2 blgp:2
	v_mov_b32_e32 v12, v122
	v_mov_b32_e32 v13, v123
	s_nop 1
	v_mfma_scale_f32_16x16x128_f8f6f4 v[102:105], v[8:13], v[26:31], v[102:105], v124, v136 op_sel_hi:[0,0,0] cbsz:2 blgp:2
	s_waitcnt lgkmcnt(4)
	v_mov_b32_e32 v36, v138
	v_mov_b32_e32 v37, v139
	s_nop 1
	v_mfma_scale_f32_16x16x128_f8f6f4 v[90:93], v[2:7], v[32:37], v[90:93], v120, v140 op_sel_hi:[0,0,0] cbsz:2 blgp:2
	s_nop 1
	v_mfma_scale_f32_16x16x128_f8f6f4 v[86:89], v[8:13], v[32:37], v[86:89], v124, v140 op_sel_hi:[0,0,0] cbsz:2 blgp:2
	s_waitcnt lgkmcnt(2)
	v_mov_b32_e32 v42, v142
	v_mov_b32_e32 v43, v143
	s_nop 1
	v_mfma_scale_f32_16x16x128_f8f6f4 v[78:81], v[2:7], v[38:43], v[78:81], v120, v144 op_sel_hi:[0,0,0] cbsz:2 blgp:2
	s_nop 1
	v_mfma_scale_f32_16x16x128_f8f6f4 v[70:73], v[8:13], v[38:43], v[70:73], v124, v144 op_sel_hi:[0,0,0] cbsz:2 blgp:2
	s_waitcnt lgkmcnt(0)
	v_mov_b32_e32 v48, v146
	v_mov_b32_e32 v49, v147
	s_nop 1
	v_mfma_scale_f32_16x16x128_f8f6f4 v[62:65], v[2:7], v[44:49], v[62:65], v120, v148 op_sel_hi:[0,0,0] cbsz:2 blgp:2
	s_nop 1
	v_mfma_scale_f32_16x16x128_f8f6f4 v[58:61], v[8:13], v[44:49], v[58:61], v124, v148 op_sel_hi:[0,0,0] cbsz:2 blgp:2
	s_setprio 1
	s_setprio 0
	v_mov_b32_e32 v18, v126
	v_mov_b32_e32 v19, v127
	s_nop 1
	v_mfma_scale_f32_16x16x128_f8f6f4 v[114:117], v[14:19], v[26:31], v[114:117], v128, v136 op_sel_hi:[0,0,0] cbsz:2 blgp:2
	v_mov_b32_e32 v24, v130
	v_mov_b32_e32 v25, v131
	s_nop 1
	v_mfma_scale_f32_16x16x128_f8f6f4 v[110:113], v[20:25], v[26:31], v[110:113], v132, v136 op_sel_hi:[0,0,0] cbsz:2 blgp:2
	s_nop 1
	v_mfma_scale_f32_16x16x128_f8f6f4 v[98:101], v[14:19], v[32:37], v[98:101], v128, v140 op_sel_hi:[0,0,0] cbsz:2 blgp:2
	s_nop 1
	v_mfma_scale_f32_16x16x128_f8f6f4 v[94:97], v[20:25], v[32:37], v[94:97], v132, v140 op_sel_hi:[0,0,0] cbsz:2 blgp:2
	s_nop 1
	v_mfma_scale_f32_16x16x128_f8f6f4 v[82:85], v[14:19], v[38:43], v[82:85], v128, v144 op_sel_hi:[0,0,0] cbsz:2 blgp:2
	s_nop 1
	v_mfma_scale_f32_16x16x128_f8f6f4 v[74:77], v[20:25], v[38:43], v[74:77], v132, v144 op_sel_hi:[0,0,0] cbsz:2 blgp:2
	s_nop 1
	v_mfma_scale_f32_16x16x128_f8f6f4 v[66:69], v[14:19], v[44:49], v[66:69], v128, v148 op_sel_hi:[0,0,0] cbsz:2 blgp:2
	s_nop 1
	v_mfma_scale_f32_16x16x128_f8f6f4 v[54:57], v[20:25], v[44:49], v[54:57], v132, v148 op_sel_hi:[0,0,0] cbsz:2 blgp:2
	s_setprio 1
	s_barrier
	s_mov_b32 s39, m0
	s_mov_b32 m0, s45
	s_nop 0
	global_load_lds_dwordx4 v153, s[50:51]
	s_mov_b32 m0, s39
	s_nop 0
	s_mov_b32 s39, m0
	s_mov_b32 m0, s62
	s_nop 0
	global_load_lds_dwordx4 v154, s[50:51]
	s_mov_b32 m0, s39
	s_add_u32 s50, s46, 0x40200
	s_addc_u32 s51, s47, 0
	s_mov_b32 s39, m0
	s_mov_b32 m0, s63
	s_nop 0
	global_load_lds_dwordx4 v153, s[50:51]
	s_mov_b32 m0, s39
	s_nop 0
	s_mov_b32 s39, m0
	s_mov_b32 m0, s64
	s_nop 0
	global_load_lds_dwordx4 v154, s[50:51]
	s_mov_b32 m0, s39
	s_nop 0
	s_mov_b32 s39, m0
	s_mov_b32 m0, s17
	s_nop 0
	global_load_lds_dwordx4 v50, s[34:35]
	s_mov_b32 m0, s39
	s_nop 0
	s_mov_b32 s39, m0
	s_mov_b32 m0, s65
	s_nop 0
	global_load_lds_dwordx4 v51, s[34:35]
	s_mov_b32 m0, s39
	s_waitcnt vmcnt(6)
	s_waitcnt lgkmcnt(0)
	s_barrier
	s_barrier
	ds_read_b128 v[2:5], v164
	ds_read_b128 v[118:121], v164 offset:1024
	ds_read_b128 v[8:11], v164 offset:2048
	ds_read_b128 v[122:125], v164 offset:3072
	ds_read_b128 v[14:17], v165
	ds_read_b128 v[126:129], v165 offset:1024
	ds_read_b128 v[20:23], v165 offset:2048
	ds_read_b128 v[130:133], v165 offset:3072
	ds_read_b128 v[26:29], v160 offset:32768
	ds_read_b128 v[134:137], v160 offset:33792
	ds_read_b128 v[32:35], v160 offset:34816
	ds_read_b128 v[138:141], v160 offset:35840
	ds_read_b128 v[38:41], v160 offset:36864
	ds_read_b128 v[142:145], v160 offset:37888
	ds_read_b128 v[44:47], v160 offset:38912
	ds_read_b128 v[146:149], v160 offset:39936
	s_waitcnt vmcnt(6)
	s_waitcnt lgkmcnt(0)
	s_barrier
; #define LAS __attribute__((address_space(3)))
; #define PG8_STAGEB(bufoff, gbase) PG8_STAGE2(bufoff, gbase, voffB[0], voffB[1])
; #define PG8_STAGEA(bufoff, gbase, h) PG8_STAGE2(bufoff, gbase, voffA[h][0], voffA[h][1])
; #define PG8_STAGEAS(bufoff, gbase, h) PG8_STAGE2(bufoff, gbase, voffA[h][0], voffA[h][1])
; #define PG8_LDA(dst, b, h) do { _Pragma("unroll") for (int m = 0; m < 4; ++m) _Pragma("unroll") for (int k = 0; k < 2; ++k) dst[m][k] = *(const LAS bf16x8*)(lds + PG8_SA(b, h) + aoff + m * 2048 + k * 1024); } while (0)
; #define PG8_LDB(dst, b, h) do { _Pragma("unroll") for (int n = 0; n < 2; ++n) _Pragma("unroll") for (int k = 0; k < 2; ++k) dst[n][k] = *(const LAS bf16x8*)(lds + PG8_SB(b, h) + boff + n * 2048 + k * 1024); } while (0)
;     ...
;             const char* a1 = cA + (size_t)(t + 1) * kstep;
;             const char* a2 = last ? nA : cA + (size_t)(t + 2) * kstep; const char* b2 = last ? nB : cB + (size_t)(t + 2) * kstep;
;             const char* a3 = a2 + kstep; const char* b3 = b2 + kstep;
;             PG8_LDB(B0, 0, 0); PG8_LDB(B1, 0, 1); PG8_SCHED; PG8_LDA(At, 0, 0); if constexpr (!HM) PG8_STAGEA(PG8_SA(1, 1), a1, 1);
;             if constexpr (Sched::kGather) { if (last && has_next) { const u32x4 tn = *(const LAS u32x4*)(S.aux + tid * 16); voffA[0][0] = tn.x; voffA[0][1] = tn.y; voffA[1][0] = tn.z; voffA[1][1] = tn.w; } }
;             PG8_WAIT_K0(); PG8_WAIT_L(0); PG8_BAR; PG8_MMA(0, 0, At, B0); PG8_MMA(0, 1, At, B1); PG8_BAR; PG8_SCHED;
;             if constexpr (!HM) PG8_LDA(At, 0, 1);
;             PG8_STAGEB(PG8_SB(0, 0), b2); PG8_STAGEB(PG8_SB(0, 1), b2 + hstepB); PG8_STAGEAS(PG8_SA(0, 0), a2, 0);
;             PG8_WAIT_K0(); PG8_WAIT_L(0); PG8_BAR; if constexpr (!HM) { PG8_MMA(1, 0, At, B0); PG8_MMA(1, 1, At, B1); } PG8_BAR; PG8_SCHED;
;             PG8_LDB(B0, 1, 0); PG8_LDB(B1, 1, 1); PG8_SCHED; PG8_LDA(At, 1, 0); if constexpr (!HM) PG8_STAGEAS(PG8_SA(0, 1), a2, 1);
;             PG8_WAIT_K(); PG8_WAIT_L(0); PG8_BAR; PG8_MMA(0, 0, At, B0); PG8_MMA(0, 1, At, B1); PG8_BAR; PG8_SCHED;
;             if constexpr (!HM) PG8_LDA(At, 1, 1);
;             PG8_STAGEB(PG8_SB(1, 0), b3); PG8_STAGEB(PG8_SB(1, 1), b3 + hstepB); PG8_STAGEAS(PG8_SA(1, 0), a3, 0);
;             PG8_WAIT_K(); PG8_WAIT_L(0); PG8_BAR; if constexpr (!HM) { PG8_MMA(1, 0, At, B0); PG8_MMA(1, 1, At, B1); } PG8_BAR; PG8_SCHED;
	s_setprio 0
	s_waitcnt lgkmcnt(6)
	v_mov_b32_e32 v30, v134
	v_mov_b32_e32 v31, v135
	v_mov_b32_e32 v6, v118
	v_mov_b32_e32 v7, v119
	s_nop 1
	v_mfma_scale_f32_16x16x128_f8f6f4 v[106:109], v[2:7], v[26:31], v[106:109], v120, v136 op_sel_hi:[0,0,0] cbsz:2 blgp:2
	v_mov_b32_e32 v12, v122
	v_mov_b32_e32 v13, v123
	s_nop 1
	v_mfma_scale_f32_16x16x128_f8f6f4 v[102:105], v[8:13], v[26:31], v[102:105], v124, v136 op_sel_hi:[0,0,0] cbsz:2 blgp:2
	s_waitcnt lgkmcnt(4)
	v_mov_b32_e32 v36, v138
	v_mov_b32_e32 v37, v139
	s_nop 1
	v_mfma_scale_f32_16x16x128_f8f6f4 v[90:93], v[2:7], v[32:37], v[90:93], v120, v140 op_sel_hi:[0,0,0] cbsz:2 blgp:2
	s_nop 1
	v_mfma_scale_f32_16x16x128_f8f6f4 v[86:89], v[8:13], v[32:37], v[86:89], v124, v140 op_sel_hi:[0,0,0] cbsz:2 blgp:2
	s_waitcnt lgkmcnt(2)
	v_mov_b32_e32 v42, v142
	v_mov_b32_e32 v43, v143
	s_nop 1
	v_mfma_scale_f32_16x16x128_f8f6f4 v[78:81], v[2:7], v[38:43], v[78:81], v120, v144 op_sel_hi:[0,0,0] cbsz:2 blgp:2
	s_nop 1
	v_mfma_scale_f32_16x16x128_f8f6f4 v[70:73], v[8:13], v[38:43], v[70:73], v124, v144 op_sel_hi:[0,0,0] cbsz:2 blgp:2
	s_waitcnt lgkmcnt(0)
	v_mov_b32_e32 v48, v146
	v_mov_b32_e32 v49, v147
	s_nop 1
	v_mfma_scale_f32_16x16x128_f8f6f4 v[62:65], v[2:7], v[44:49], v[62:65], v120, v148 op_sel_hi:[0,0,0] cbsz:2 blgp:2
	s_nop 1
	v_mfma_scale_f32_16x16x128_f8f6f4 v[58:61], v[8:13], v[44:49], v[58:61], v124, v148 op_sel_hi:[0,0,0] cbsz:2 blgp:2
	s_setprio 1
	s_setprio 0
	v_mov_b32_e32 v18, v126
	v_mov_b32_e32 v19, v127
	s_nop 1
	v_mfma_scale_f32_16x16x128_f8f6f4 v[114:117], v[14:19], v[26:31], v[114:117], v128, v136 op_sel_hi:[0,0,0] cbsz:2 blgp:2
	v_mov_b32_e32 v24, v130
	v_mov_b32_e32 v25, v131
	s_nop 1
	v_mfma_scale_f32_16x16x128_f8f6f4 v[110:113], v[20:25], v[26:31], v[110:113], v132, v136 op_sel_hi:[0,0,0] cbsz:2 blgp:2
	s_nop 1
	v_mfma_scale_f32_16x16x128_f8f6f4 v[98:101], v[14:19], v[32:37], v[98:101], v128, v140 op_sel_hi:[0,0,0] cbsz:2 blgp:2
	s_nop 1
	v_mfma_scale_f32_16x16x128_f8f6f4 v[94:97], v[20:25], v[32:37], v[94:97], v132, v140 op_sel_hi:[0,0,0] cbsz:2 blgp:2
	s_nop 1
	v_mfma_scale_f32_16x16x128_f8f6f4 v[82:85], v[14:19], v[38:43], v[82:85], v128, v144 op_sel_hi:[0,0,0] cbsz:2 blgp:2
	s_nop 1
	v_mfma_scale_f32_16x16x128_f8f6f4 v[74:77], v[20:25], v[38:43], v[74:77], v132, v144 op_sel_hi:[0,0,0] cbsz:2 blgp:2
	s_nop 1
	v_mfma_scale_f32_16x16x128_f8f6f4 v[66:69], v[14:19], v[44:49], v[66:69], v128, v148 op_sel_hi:[0,0,0] cbsz:2 blgp:2
	s_nop 1
	v_mfma_scale_f32_16x16x128_f8f6f4 v[54:57], v[20:25], v[44:49], v[54:57], v132, v148 op_sel_hi:[0,0,0] cbsz:2 blgp:2
	s_setprio 1
	s_barrier
	s_mov_b32 s39, m0
	s_mov_b32 m0, s66
	s_nop 0
	global_load_lds_dwordx4 v153, s[48:49]
	s_mov_b32 m0, s39
	s_nop 0
	s_mov_b32 s39, m0
	s_mov_b32 m0, s67
	s_nop 0
	global_load_lds_dwordx4 v154, s[48:49]
	s_mov_b32 m0, s39
	s_add_u32 s48, s46, 0x40280
	s_addc_u32 s49, s47, 0
	s_mov_b32 s39, m0
	s_mov_b32 m0, s70
	s_nop 0
	global_load_lds_dwordx4 v153, s[48:49]
	s_mov_b32 m0, s39
	s_nop 0
	s_mov_b32 s39, m0
	s_mov_b32 m0, s71
	s_nop 0
	global_load_lds_dwordx4 v154, s[48:49]
	s_mov_b32 m0, s39
	s_nop 0
	s_mov_b32 s39, m0
	s_mov_b32 m0, s68
	s_nop 0
	global_load_lds_dwordx4 v50, s[36:37]
	s_mov_b32 m0, s39
	s_nop 0
	s_mov_b32 s39, m0
	s_mov_b32 m0, s69
	s_nop 0
	global_load_lds_dwordx4 v51, s[36:37]
	s_mov_b32 m0, s39
	s_waitcnt vmcnt(6)
	s_waitcnt lgkmcnt(0)
	s_barrier
	s_barrier
	s_mov_b32 s39, 2
	s_mov_b64 s[48:49], 0x300
	s_branch .LBB0_1188
.LBB0_1187:
	s_and_b64 s[50:51], s[52:53], exec
	s_cselect_b32 s50, 0, s48
	s_cselect_b32 s41, 0, s49
	s_add_u32 s56, s0, s50
	s_addc_u32 s57, s1, s41
	s_add_u32 s41, s46, s48
	s_addc_u32 s54, s47, s49
	s_add_u32 s50, s56, 0x80
	s_addc_u32 s51, s57, 0
	s_waitcnt vmcnt(6)
	s_and_b64 s[52:53], s[52:53], exec
	s_waitcnt lgkmcnt(0)
	s_cselect_b32 s52, s42, s41
	s_cselect_b32 s53, s43, s54
	s_add_u32 s54, s52, 0x80
	s_addc_u32 s55, s53, 0
	s_barrier
	s_setprio 0
	s_waitcnt lgkmcnt(6)
	v_mov_b32_e32 v36, v138
	v_mov_b32_e32 v37, v139
	v_mov_b32_e32 v48, v146
	v_mov_b32_e32 v49, v147
	s_nop 1
	v_mfma_scale_f32_16x16x128_f8f6f4 v[106:109], v[44:49], v[32:37], v[106:109], v148, v140 op_sel_hi:[0,0,0] cbsz:2 blgp:2
	v_mov_b32_e32 v42, v142
	v_mov_b32_e32 v43, v143
	s_nop 1
	v_mfma_scale_f32_16x16x128_f8f6f4 v[102:105], v[38:43], v[32:37], v[102:105], v144, v140 op_sel_hi:[0,0,0] cbsz:2 blgp:2
	s_waitcnt lgkmcnt(4)
	v_mov_b32_e32 v30, v134
	v_mov_b32_e32 v31, v135
	s_nop 1
	v_mfma_scale_f32_16x16x128_f8f6f4 v[90:93], v[44:49], v[26:31], v[90:93], v148, v136 op_sel_hi:[0,0,0] cbsz:2 blgp:2
	s_nop 1
	v_mfma_scale_f32_16x16x128_f8f6f4 v[86:89], v[38:43], v[26:31], v[86:89], v144, v136 op_sel_hi:[0,0,0] cbsz:2 blgp:2
	s_waitcnt lgkmcnt(2)
	v_mov_b32_e32 v24, v130
	v_mov_b32_e32 v25, v131
	s_nop 1
	v_mfma_scale_f32_16x16x128_f8f6f4 v[78:81], v[44:49], v[20:25], v[78:81], v148, v132 op_sel_hi:[0,0,0] cbsz:2 blgp:2
	s_nop 1
	v_mfma_scale_f32_16x16x128_f8f6f4 v[70:73], v[38:43], v[20:25], v[70:73], v144, v132 op_sel_hi:[0,0,0] cbsz:2 blgp:2
	s_waitcnt lgkmcnt(0)
	v_mov_b32_e32 v18, v126
	v_mov_b32_e32 v19, v127
	s_nop 1
	v_mfma_scale_f32_16x16x128_f8f6f4 v[62:65], v[44:49], v[14:19], v[62:65], v148, v128 op_sel_hi:[0,0,0] cbsz:2 blgp:2
	s_nop 1
	v_mfma_scale_f32_16x16x128_f8f6f4 v[58:61], v[38:43], v[14:19], v[58:61], v144, v128 op_sel_hi:[0,0,0] cbsz:2 blgp:2
	s_setprio 1
	s_setprio 0
	v_mov_b32_e32 v12, v122
	v_mov_b32_e32 v13, v123
	s_nop 1
	v_mfma_scale_f32_16x16x128_f8f6f4 v[114:117], v[8:13], v[32:37], v[114:117], v124, v140 op_sel_hi:[0,0,0] cbsz:2 blgp:2
	v_mov_b32_e32 v6, v118
	v_mov_b32_e32 v7, v119
	s_nop 1
	v_mfma_scale_f32_16x16x128_f8f6f4 v[110:113], v[2:7], v[32:37], v[110:113], v120, v140 op_sel_hi:[0,0,0] cbsz:2 blgp:2
	s_nop 1
	v_mfma_scale_f32_16x16x128_f8f6f4 v[98:101], v[8:13], v[26:31], v[98:101], v124, v136 op_sel_hi:[0,0,0] cbsz:2 blgp:2
	s_nop 1
	v_mfma_scale_f32_16x16x128_f8f6f4 v[94:97], v[2:7], v[26:31], v[94:97], v120, v136 op_sel_hi:[0,0,0] cbsz:2 blgp:2
	s_nop 1
	v_mfma_scale_f32_16x16x128_f8f6f4 v[82:85], v[8:13], v[20:25], v[82:85], v124, v132 op_sel_hi:[0,0,0] cbsz:2 blgp:2
	s_nop 1
	v_mfma_scale_f32_16x16x128_f8f6f4 v[74:77], v[2:7], v[20:25], v[74:77], v120, v132 op_sel_hi:[0,0,0] cbsz:2 blgp:2
	s_nop 1
	v_mfma_scale_f32_16x16x128_f8f6f4 v[66:69], v[8:13], v[14:19], v[66:69], v124, v128 op_sel_hi:[0,0,0] cbsz:2 blgp:2
	s_nop 1
	v_mfma_scale_f32_16x16x128_f8f6f4 v[54:57], v[2:7], v[14:19], v[54:57], v120, v128 op_sel_hi:[0,0,0] cbsz:2 blgp:2
	s_setprio 1
	s_barrier
; #define PG8_STAGEB(bufoff, gbase) PG8_STAGE2(bufoff, gbase, voffB[0], voffB[1])
; #define PG8_STAGEAS(bufoff, gbase, h) PG8_STAGE2(bufoff, gbase, voffA[h][0], voffA[h][1])
; #define PG8_LDA(dst, b, h) do { _Pragma("unroll") for (int m = 0; m < 4; ++m) _Pragma("unroll") for (int k = 0; k < 2; ++k) dst[m][k] = *(const LAS bf16x8*)(lds + PG8_SA(b, h) + aoff + m * 2048 + k * 1024); } while (0)
; #define PG8_WAIT_K() do { if constexpr (HM) PG8_WAIT_V(6); else PG8_WAIT_V(8); } while (0)
; #define PG8_WAIT_L(n) asm volatile("s_waitcnt lgkmcnt(" #n ")" ::: "memory")
; #define PG8_BAR __builtin_amdgcn_s_barrier()
; #define PG8_SCHED __builtin_amdgcn_sched_barrier(0)
;     ...
;             PG8_WAIT_K(); PG8_WAIT_L(0); PG8_BAR; PG8_MMA(0, 0, At, B0); PG8_MMA(0, 1, At, B1); PG8_BAR; PG8_SCHED;
;             if constexpr (!HM) PG8_LDA(At, 1, 1);
;             PG8_STAGEB(PG8_SB(1, 0), b3); PG8_STAGEB(PG8_SB(1, 1), b3 + hstepB); PG8_STAGEAS(PG8_SA(1, 0), a3, 0);
;             PG8_WAIT_K(); PG8_WAIT_L(0); PG8_BAR; if constexpr (!HM) { PG8_MMA(1, 0, At, B0); PG8_MMA(1, 1, At, B1); } PG8_BAR; PG8_SCHED;
	s_mov_b32 s41, m0
	s_mov_b32 m0, s45
	s_nop 0
	global_load_lds_dwordx4 v153, s[52:53]
	s_mov_b32 m0, s41
	s_add_u32 s78, s52, 0x40000
	s_mov_b32 s41, m0
	s_mov_b32 m0, s62
	s_nop 0
	global_load_lds_dwordx4 v154, s[52:53]
	s_mov_b32 m0, s41
	s_addc_u32 s79, s53, 0
	s_mov_b32 s41, m0
	s_mov_b32 m0, s63
	s_nop 0
	global_load_lds_dwordx4 v153, s[78:79]
	s_mov_b32 m0, s41
	s_nop 0
	s_mov_b32 s41, m0
	s_mov_b32 m0, s64
	s_nop 0
	global_load_lds_dwordx4 v154, s[78:79]
	s_mov_b32 m0, s41
	s_nop 0
	s_mov_b32 s41, m0
	s_mov_b32 m0, s17
	s_nop 0
	global_load_lds_dwordx4 v50, s[56:57]
	s_mov_b32 m0, s41
	s_nop 0
	s_mov_b32 s41, m0
	s_mov_b32 m0, s65
	s_nop 0
	global_load_lds_dwordx4 v51, s[56:57]
	s_mov_b32 m0, s41
	s_waitcnt vmcnt(6)
	s_waitcnt lgkmcnt(0)
	s_barrier
	s_barrier
	ds_read_b128 v[2:5], v164
	ds_read_b128 v[118:121], v164 offset:1024
	ds_read_b128 v[8:11], v164 offset:2048
	ds_read_b128 v[122:125], v164 offset:3072
	ds_read_b128 v[14:17], v165
	ds_read_b128 v[126:129], v165 offset:1024
	ds_read_b128 v[20:23], v165 offset:2048
	ds_read_b128 v[130:133], v165 offset:3072
	ds_read_b128 v[26:29], v160 offset:32768
	ds_read_b128 v[134:137], v160 offset:33792
	ds_read_b128 v[32:35], v160 offset:34816
	ds_read_b128 v[138:141], v160 offset:35840
	ds_read_b128 v[38:41], v160 offset:36864
	ds_read_b128 v[142:145], v160 offset:37888
	ds_read_b128 v[44:47], v160 offset:38912
	ds_read_b128 v[146:149], v160 offset:39936
	s_waitcnt vmcnt(6)
	s_waitcnt lgkmcnt(0)
	s_barrier
	s_setprio 0
	s_waitcnt lgkmcnt(6)
	v_mov_b32_e32 v30, v134
	v_mov_b32_e32 v31, v135
	v_mov_b32_e32 v6, v118
	v_mov_b32_e32 v7, v119
	s_nop 1
	v_mfma_scale_f32_16x16x128_f8f6f4 v[106:109], v[2:7], v[26:31], v[106:109], v120, v136 op_sel_hi:[0,0,0] cbsz:2 blgp:2
	v_mov_b32_e32 v12, v122
	v_mov_b32_e32 v13, v123
	s_nop 1
	v_mfma_scale_f32_16x16x128_f8f6f4 v[102:105], v[8:13], v[26:31], v[102:105], v124, v136 op_sel_hi:[0,0,0] cbsz:2 blgp:2
	s_waitcnt lgkmcnt(4)
	v_mov_b32_e32 v36, v138
	v_mov_b32_e32 v37, v139
	s_nop 1
	v_mfma_scale_f32_16x16x128_f8f6f4 v[90:93], v[2:7], v[32:37], v[90:93], v120, v140 op_sel_hi:[0,0,0] cbsz:2 blgp:2
	s_nop 1
	v_mfma_scale_f32_16x16x128_f8f6f4 v[86:89], v[8:13], v[32:37], v[86:89], v124, v140 op_sel_hi:[0,0,0] cbsz:2 blgp:2
	s_waitcnt lgkmcnt(2)
	v_mov_b32_e32 v42, v142
	v_mov_b32_e32 v43, v143
	s_nop 1
	v_mfma_scale_f32_16x16x128_f8f6f4 v[78:81], v[2:7], v[38:43], v[78:81], v120, v144 op_sel_hi:[0,0,0] cbsz:2 blgp:2
	s_nop 1
	v_mfma_scale_f32_16x16x128_f8f6f4 v[70:73], v[8:13], v[38:43], v[70:73], v124, v144 op_sel_hi:[0,0,0] cbsz:2 blgp:2
	s_waitcnt lgkmcnt(0)
	v_mov_b32_e32 v48, v146
	v_mov_b32_e32 v49, v147
	s_nop 1
	v_mfma_scale_f32_16x16x128_f8f6f4 v[62:65], v[2:7], v[44:49], v[62:65], v120, v148 op_sel_hi:[0,0,0] cbsz:2 blgp:2
	s_nop 1
	v_mfma_scale_f32_16x16x128_f8f6f4 v[58:61], v[8:13], v[44:49], v[58:61], v124, v148 op_sel_hi:[0,0,0] cbsz:2 blgp:2
	s_setprio 1
	s_setprio 0
	v_mov_b32_e32 v18, v126
	v_mov_b32_e32 v19, v127
	s_nop 1
	v_mfma_scale_f32_16x16x128_f8f6f4 v[114:117], v[14:19], v[26:31], v[114:117], v128, v136 op_sel_hi:[0,0,0] cbsz:2 blgp:2
	v_mov_b32_e32 v24, v130
	v_mov_b32_e32 v25, v131
	s_nop 1
	v_mfma_scale_f32_16x16x128_f8f6f4 v[110:113], v[20:25], v[26:31], v[110:113], v132, v136 op_sel_hi:[0,0,0] cbsz:2 blgp:2
	s_nop 1
	v_mfma_scale_f32_16x16x128_f8f6f4 v[98:101], v[14:19], v[32:37], v[98:101], v128, v140 op_sel_hi:[0,0,0] cbsz:2 blgp:2
	s_nop 1
	v_mfma_scale_f32_16x16x128_f8f6f4 v[94:97], v[20:25], v[32:37], v[94:97], v132, v140 op_sel_hi:[0,0,0] cbsz:2 blgp:2
	s_nop 1
	v_mfma_scale_f32_16x16x128_f8f6f4 v[82:85], v[14:19], v[38:43], v[82:85], v128, v144 op_sel_hi:[0,0,0] cbsz:2 blgp:2
	s_nop 1
	v_mfma_scale_f32_16x16x128_f8f6f4 v[74:77], v[20:25], v[38:43], v[74:77], v132, v144 op_sel_hi:[0,0,0] cbsz:2 blgp:2
	s_nop 1
	v_mfma_scale_f32_16x16x128_f8f6f4 v[66:69], v[14:19], v[44:49], v[66:69], v128, v148 op_sel_hi:[0,0,0] cbsz:2 blgp:2
	s_nop 1
	v_mfma_scale_f32_16x16x128_f8f6f4 v[54:57], v[20:25], v[44:49], v[54:57], v132, v148 op_sel_hi:[0,0,0] cbsz:2 blgp:2
	s_setprio 1
	s_barrier
	s_mov_b32 s41, m0
	s_mov_b32 m0, s66
	s_nop 0
	global_load_lds_dwordx4 v153, s[54:55]
	s_mov_b32 m0, s41
	s_add_u32 s52, s52, 0x40080
	s_mov_b32 s41, m0
	s_mov_b32 m0, s67
	s_nop 0
	global_load_lds_dwordx4 v154, s[54:55]
	s_mov_b32 m0, s41
	s_addc_u32 s53, s53, 0
	s_mov_b32 s41, m0
	s_mov_b32 m0, s70
	s_nop 0
	global_load_lds_dwordx4 v153, s[52:53]
	s_mov_b32 m0, s41
	s_nop 0
	s_mov_b32 s41, m0
	s_mov_b32 m0, s71
	s_nop 0
	global_load_lds_dwordx4 v154, s[52:53]
	s_mov_b32 m0, s41
	s_nop 0
	s_mov_b32 s41, m0
	s_mov_b32 m0, s68
	s_nop 0
	global_load_lds_dwordx4 v50, s[50:51]
	s_mov_b32 m0, s41
	s_nop 0
	s_mov_b32 s41, m0
	s_mov_b32 m0, s69
	s_nop 0
	global_load_lds_dwordx4 v51, s[50:51]
	s_mov_b32 m0, s41
	s_waitcnt vmcnt(6)
	s_waitcnt lgkmcnt(0)
	s_barrier
	s_barrier
	s_add_i32 s39, s39, 2
	s_add_u32 s48, s48, 0x100
	s_addc_u32 s49, s49, 0
	s_cmp_gt_u32 s39, 13
	s_cbranch_scc1 .LBB0_1190
